# adds: GEMM K-loop LDS-DMA loads use SGPR base + 32-bit lane offset (26 64-bit VALU address adds removed per trip set)
# speedup vs baseline: 1.0043x; 1.0025x over previous
; #define PG8_STAGE(bufoff, gbase, voff) do { _Pragma("unroll") for (int _i = 0; _i < 2; ++_i) \
;         __builtin_amdgcn_global_load_lds((const unsigned*)((const char*)(gbase) + (voff)[_i]), (PG8_LAS unsigned*)(lds + (bufoff) + ldsw + _i * 8192), 16, 0, 0); } while (0)
; #define PG8_STAGE_A(bufoff, gbase, OA, h) do { _Pragma("unroll") for (int _i = 0; _i < 2; ++_i) \
;         __builtin_amdgcn_global_load_lds((const unsigned*)((const char*)(gbase) + (OA)[h][_i]), (PG8_LAS unsigned*)(lds + (bufoff) + ldsw + _i * 8192), 16, 0, 0); } while (0)
; #define PG8_WAIT_V(n) asm volatile("s_waitcnt vmcnt(" #n ")" ::: "memory")
; #define PG8_WAIT_L(n) asm volatile("s_waitcnt lgkmcnt(" #n ")" ::: "memory")
; #define PG8_BAR __builtin_amdgcn_s_barrier()
; #define PG8_SCHED __builtin_amdgcn_sched_barrier(0)
;     ...
;             PG8_LDB(B0, 0, 0); PG8_LDB(B1, 0, 1); PG8_SCHED; PG8_LDA(At, 0, 0); PG8_STAGE_A(PG8_SA(1, 1), a1, oc, 1);
;             PG8_WAIT_V(8); PG8_WAIT_L(0); PG8_BAR; PG8_MMA(0, 0, At, B0); PG8_MMA(0, 1, At, B1); PG8_BAR; PG8_SCHED;
;             PG8_LDA(At, 0, 1); PG8_STAGE(PG8_SB(0, 0), b2, voffB); PG8_STAGE(PG8_SB(0, 1), b2 + hstep, voffB); PG8_STAGE_A(PG8_SA(0, 0), a2, o2, 0);
;             PG8_WAIT_V(8); PG8_WAIT_L(0); PG8_BAR; PG8_MMA(1, 0, At, B0); PG8_MMA(1, 1, At, B1); PG8_BAR; PG8_SCHED;
.LBB0_179:
	v_add_u32_e32 v142, s89, v145
	ds_read_b128 v[148:151], v142
	ds_read_b128 v[152:155], v142 offset:1024
	ds_read_b128 v[156:159], v142 offset:2048
	ds_read_b128 v[160:163], v142 offset:3072
	v_add_u32_e32 v142, s49, v145
	ds_read_b128 v[164:167], v142
	ds_read_b128 v[168:171], v142 offset:1024
	ds_read_b128 v[172:175], v142 offset:2048
	ds_read_b128 v[176:179], v142 offset:3072
	s_add_u32 s0, s14, 0x80
	s_addc_u32 s1, s15, 0
	s_cmp_eq_u32 s21, 12
	s_cselect_b32 s3, s27, s1
	s_cselect_b32 s2, s26, s0
	s_cselect_b32 s1, s25, s5
	s_cselect_b32 s0, s24, s4
	s_add_i32 m0, s42, 0xc000
	ds_read_b128 v[182:185], v146
	ds_read_b128 v[186:189], v146 offset:1024
	ds_read_b128 v[190:193], v146 offset:2048
	ds_read_b128 v[194:197], v146 offset:3072
	ds_read_b128 v[202:205], v146 offset:4096
	ds_read_b128 v[206:209], v146 offset:5120
	ds_read_b128 v[220:223], v146 offset:6144
	ds_read_b128 v[224:227], v146 offset:7168
	global_load_lds_dwordx4 v140, s[14:15]
	s_add_i32 m0, s42, 0xe000
	s_nop 0
	global_load_lds_dwordx4 v138, s[14:15]
	s_waitcnt vmcnt(8)
	s_waitcnt lgkmcnt(0)
	s_barrier
	s_setprio 1
	s_waitcnt lgkmcnt(0)
	v_mfma_f32_16x16x32_bf16 v[124:127], v[148:151], v[182:185], v[124:127]
	v_mfma_f32_16x16x32_bf16 v[120:123], v[156:159], v[182:185], v[120:123]
	v_mfma_f32_16x16x32_bf16 v[116:119], v[148:151], v[190:193], v[116:119]
	v_mfma_f32_16x16x32_bf16 v[108:111], v[156:159], v[190:193], v[108:111]
	v_mfma_f32_16x16x32_bf16 v[100:103], v[148:151], v[202:205], v[100:103]
	v_mfma_f32_16x16x32_bf16 v[92:95], v[156:159], v[202:205], v[92:95]
	v_mfma_f32_16x16x32_bf16 v[84:87], v[148:151], v[220:223], v[84:87]
	v_mfma_f32_16x16x32_bf16 v[76:79], v[156:159], v[220:223], v[76:79]
	v_mfma_f32_16x16x32_bf16 v[124:127], v[152:155], v[186:189], v[124:127]
	v_mfma_f32_16x16x32_bf16 v[120:123], v[160:163], v[186:189], v[120:123]
	v_mfma_f32_16x16x32_bf16 v[116:119], v[152:155], v[194:197], v[116:119]
	v_mfma_f32_16x16x32_bf16 v[108:111], v[160:163], v[194:197], v[108:111]
	v_mfma_f32_16x16x32_bf16 v[100:103], v[152:155], v[206:209], v[100:103]
	v_mfma_f32_16x16x32_bf16 v[92:95], v[160:163], v[206:209], v[92:95]
	v_mfma_f32_16x16x32_bf16 v[84:87], v[152:155], v[224:227], v[84:87]
	v_mfma_f32_16x16x32_bf16 v[76:79], v[160:163], v[224:227], v[76:79]
	s_setprio 0
	s_setprio 1
	v_mfma_f32_16x16x32_bf16 v[112:115], v[164:167], v[182:185], v[112:115]
	v_mfma_f32_16x16x32_bf16 v[104:107], v[172:175], v[182:185], v[104:107]
	v_mfma_f32_16x16x32_bf16 v[96:99], v[164:167], v[190:193], v[96:99]
	v_mfma_f32_16x16x32_bf16 v[88:91], v[172:175], v[190:193], v[88:91]
	v_mfma_f32_16x16x32_bf16 v[80:83], v[164:167], v[202:205], v[80:83]
	v_mfma_f32_16x16x32_bf16 v[72:75], v[172:175], v[202:205], v[72:75]
	v_mfma_f32_16x16x32_bf16 v[68:71], v[164:167], v[220:223], v[68:71]
	v_mfma_f32_16x16x32_bf16 v[64:67], v[172:175], v[220:223], v[64:67]
	v_mfma_f32_16x16x32_bf16 v[112:115], v[168:171], v[186:189], v[112:115]
	v_mfma_f32_16x16x32_bf16 v[104:107], v[176:179], v[186:189], v[104:107]
	v_mfma_f32_16x16x32_bf16 v[96:99], v[168:171], v[194:197], v[96:99]
	v_mfma_f32_16x16x32_bf16 v[88:91], v[176:179], v[194:197], v[88:91]
	v_mfma_f32_16x16x32_bf16 v[80:83], v[168:171], v[206:209], v[80:83]
	v_mfma_f32_16x16x32_bf16 v[72:75], v[176:179], v[206:209], v[72:75]
	v_mfma_f32_16x16x32_bf16 v[68:71], v[168:171], v[224:227], v[68:71]
	v_mfma_f32_16x16x32_bf16 v[64:67], v[176:179], v[224:227], v[64:67]
	s_setprio 0
	s_barrier
	s_add_i32 s23, s89, s28
	v_lshl_add_u64 v[142:143], s[0:1], 0, v[180:181]
	s_mov_b32 m0, s23
	ds_read_b128 v[182:185], v146 offset:16384
	ds_read_b128 v[186:189], v146 offset:17408
	ds_read_b128 v[190:193], v146 offset:18432
	ds_read_b128 v[194:197], v146 offset:19456
	ds_read_b128 v[202:205], v146 offset:20480
	ds_read_b128 v[206:209], v146 offset:21504
	ds_read_b128 v[220:223], v146 offset:22528
	ds_read_b128 v[224:227], v146 offset:23552
	global_load_lds_dwordx4 v180, s[0:1]
	s_add_i32 m0, s23, 0x2000
	s_add_u32 s40, s0, 0x40000
	v_lshl_add_u64 v[198:199], s[0:1], 0, v[132:133]
	s_addc_u32 s41, s1, 0
	s_add_i32 s23, s49, s28
	global_load_lds_dwordx4 v132, s[0:1]
	s_mov_b32 m0, s23
	v_lshl_add_u64 v[230:231], s[2:3], 0, v[128:129]
	global_load_lds_dwordx4 v180, s[40:41]
	s_add_i32 m0, s23, 0x2000
	s_nop 0
	global_load_lds_dwordx4 v132, s[40:41]
	v_lshl_add_u64 v[228:229], s[2:3], 0, v[134:135]
	s_mov_b32 m0, s42
	s_nop 0
	global_load_lds_dwordx4 v134, s[2:3]
	s_add_i32 m0, s42, 0x2000
	s_nop 0
	global_load_lds_dwordx4 v128, s[2:3]
	s_waitcnt vmcnt(8)
	s_waitcnt lgkmcnt(0)
	s_barrier
; #define PG8_STAGE(bufoff, gbase, voff) do { _Pragma("unroll") for (int _i = 0; _i < 2; ++_i) \
;         __builtin_amdgcn_global_load_lds((const unsigned*)((const char*)(gbase) + (voff)[_i]), (PG8_LAS unsigned*)(lds + (bufoff) + ldsw + _i * 8192), 16, 0, 0); } while (0)
; #define PG8_STAGE_A(bufoff, gbase, OA, h) do { _Pragma("unroll") for (int _i = 0; _i < 2; ++_i) \
;         __builtin_amdgcn_global_load_lds((const unsigned*)((const char*)(gbase) + (OA)[h][_i]), (PG8_LAS unsigned*)(lds + (bufoff) + ldsw + _i * 8192), 16, 0, 0); } while (0)
; #define PG8_WAIT_V(n) asm volatile("s_waitcnt vmcnt(" #n ")" ::: "memory")
; #define PG8_WAIT_L(n) asm volatile("s_waitcnt lgkmcnt(" #n ")" ::: "memory")
; #define PG8_BAR __builtin_amdgcn_s_barrier()
; #define PG8_SCHED __builtin_amdgcn_sched_barrier(0)
;     ...
;             PG8_WAIT_V(8); PG8_WAIT_L(0); PG8_BAR; PG8_MMA(1, 0, At, B0); PG8_MMA(1, 1, At, B1); PG8_BAR; PG8_SCHED;
;             PG8_LDB(B0, 1, 0); PG8_LDB(B1, 1, 1); PG8_SCHED; PG8_LDA(At, 1, 0); PG8_STAGE_A(PG8_SA(0, 1), a2, o2, 1);
;             PG8_WAIT_V(8); PG8_WAIT_L(0); PG8_BAR; PG8_MMA(0, 0, At, B0); PG8_MMA(0, 1, At, B1); PG8_BAR; PG8_SCHED;
;             PG8_LDA(At, 1, 1); PG8_STAGE(PG8_SB(1, 0), b3, voffB); PG8_STAGE(PG8_SB(1, 1), b3 + hstep, voffB); PG8_STAGE_A(PG8_SA(1, 0), a3, o2, 0);
;             PG8_WAIT_V(8); PG8_WAIT_L(0); PG8_BAR; PG8_MMA(1, 0, At, B0); PG8_MMA(1, 1, At, B1); PG8_BAR; PG8_SCHED;
	s_setprio 1
	s_waitcnt lgkmcnt(0)
	v_mfma_f32_16x16x32_bf16 v[60:63], v[148:151], v[182:185], v[60:63]
	v_mfma_f32_16x16x32_bf16 v[56:59], v[156:159], v[182:185], v[56:59]
	v_mfma_f32_16x16x32_bf16 v[44:47], v[148:151], v[190:193], v[44:47]
	v_mfma_f32_16x16x32_bf16 v[36:39], v[156:159], v[190:193], v[36:39]
	v_mfma_f32_16x16x32_bf16 v[20:23], v[148:151], v[202:205], v[20:23]
	v_mfma_f32_16x16x32_bf16 v[12:15], v[156:159], v[202:205], v[12:15]
	v_mfma_f32_16x16x32_bf16 v[4:7], v[148:151], v[220:223], v[4:7]
	v_mfma_f32_16x16x32_bf16 v[0:3], v[156:159], v[220:223], v[0:3]
	v_mfma_f32_16x16x32_bf16 v[60:63], v[152:155], v[186:189], v[60:63]
	v_mfma_f32_16x16x32_bf16 v[56:59], v[160:163], v[186:189], v[56:59]
	v_mfma_f32_16x16x32_bf16 v[44:47], v[152:155], v[194:197], v[44:47]
	v_mfma_f32_16x16x32_bf16 v[36:39], v[160:163], v[194:197], v[36:39]
	v_mfma_f32_16x16x32_bf16 v[20:23], v[152:155], v[206:209], v[20:23]
	v_mfma_f32_16x16x32_bf16 v[12:15], v[160:163], v[206:209], v[12:15]
	v_mfma_f32_16x16x32_bf16 v[4:7], v[152:155], v[224:227], v[4:7]
	v_mfma_f32_16x16x32_bf16 v[0:3], v[160:163], v[224:227], v[0:3]
	s_setprio 0
	s_setprio 1
	v_mfma_f32_16x16x32_bf16 v[40:43], v[164:167], v[182:185], v[40:43]
	v_mfma_f32_16x16x32_bf16 v[32:35], v[172:175], v[182:185], v[32:35]
	v_mfma_f32_16x16x32_bf16 v[16:19], v[164:167], v[190:193], v[16:19]
	v_mfma_f32_16x16x32_bf16 v[8:11], v[172:175], v[190:193], v[8:11]
	v_mfma_f32_16x16x32_bf16 v[52:55], v[164:167], v[202:205], v[52:55]
	v_mfma_f32_16x16x32_bf16 v[48:51], v[172:175], v[202:205], v[48:51]
	v_mfma_f32_16x16x32_bf16 v[28:31], v[164:167], v[220:223], v[28:31]
	v_mfma_f32_16x16x32_bf16 v[24:27], v[172:175], v[220:223], v[24:27]
	v_mfma_f32_16x16x32_bf16 v[40:43], v[168:171], v[186:189], v[40:43]
	v_mfma_f32_16x16x32_bf16 v[32:35], v[176:179], v[186:189], v[32:35]
	v_mfma_f32_16x16x32_bf16 v[16:19], v[168:171], v[194:197], v[16:19]
	v_mfma_f32_16x16x32_bf16 v[8:11], v[176:179], v[194:197], v[8:11]
	v_mfma_f32_16x16x32_bf16 v[52:55], v[168:171], v[206:209], v[52:55]
	v_mfma_f32_16x16x32_bf16 v[48:51], v[176:179], v[206:209], v[48:51]
	v_mfma_f32_16x16x32_bf16 v[28:31], v[168:171], v[224:227], v[28:31]
	v_mfma_f32_16x16x32_bf16 v[24:27], v[176:179], v[224:227], v[24:27]
	s_setprio 0
	s_barrier
	s_add_i32 s23, 0, 0x18000
	v_add_u32_e32 v147, s23, v145
	s_add_i32 s40, 0, 0x1c000
	ds_read_b128 v[148:151], v147
	ds_read_b128 v[152:155], v147 offset:1024
	ds_read_b128 v[156:159], v147 offset:2048
	ds_read_b128 v[160:163], v147 offset:3072
	v_add_u32_e32 v147, s40, v145
	ds_read_b128 v[164:167], v147
	ds_read_b128 v[168:171], v147 offset:1024
	ds_read_b128 v[172:175], v147 offset:2048
	ds_read_b128 v[176:179], v147 offset:3072
	s_add_i32 m0, s42, 0x4000
	ds_read_b128 v[182:185], v146 offset:32768
	ds_read_b128 v[186:189], v146 offset:33792
	ds_read_b128 v[190:193], v146 offset:34816
	ds_read_b128 v[194:197], v146 offset:35840
	ds_read_b128 v[202:205], v146 offset:36864
	ds_read_b128 v[206:209], v146 offset:37888
	ds_read_b128 v[220:223], v146 offset:38912
	ds_read_b128 v[224:227], v146 offset:39936
	global_load_lds_dwordx4 v136, s[2:3]
	s_add_i32 m0, s42, 0x6000
	s_nop 0
	global_load_lds_dwordx4 v130, s[2:3]
	s_waitcnt vmcnt(8)
	s_waitcnt lgkmcnt(0)
	s_barrier
	s_setprio 1
	s_waitcnt lgkmcnt(0)
	v_mfma_f32_16x16x32_bf16 v[124:127], v[148:151], v[182:185], v[124:127]
	v_mfma_f32_16x16x32_bf16 v[120:123], v[156:159], v[182:185], v[120:123]
	v_mfma_f32_16x16x32_bf16 v[116:119], v[148:151], v[190:193], v[116:119]
	v_mfma_f32_16x16x32_bf16 v[108:111], v[156:159], v[190:193], v[108:111]
	v_mfma_f32_16x16x32_bf16 v[100:103], v[148:151], v[202:205], v[100:103]
	v_mfma_f32_16x16x32_bf16 v[92:95], v[156:159], v[202:205], v[92:95]
	v_mfma_f32_16x16x32_bf16 v[84:87], v[148:151], v[220:223], v[84:87]
	v_mfma_f32_16x16x32_bf16 v[76:79], v[156:159], v[220:223], v[76:79]
	v_mfma_f32_16x16x32_bf16 v[124:127], v[152:155], v[186:189], v[124:127]
	v_mfma_f32_16x16x32_bf16 v[120:123], v[160:163], v[186:189], v[120:123]
	v_mfma_f32_16x16x32_bf16 v[116:119], v[152:155], v[194:197], v[116:119]
	v_mfma_f32_16x16x32_bf16 v[108:111], v[160:163], v[194:197], v[108:111]
	v_mfma_f32_16x16x32_bf16 v[100:103], v[152:155], v[206:209], v[100:103]
	v_mfma_f32_16x16x32_bf16 v[92:95], v[160:163], v[206:209], v[92:95]
	v_mfma_f32_16x16x32_bf16 v[84:87], v[152:155], v[224:227], v[84:87]
	v_mfma_f32_16x16x32_bf16 v[76:79], v[160:163], v[224:227], v[76:79]
	s_setprio 0
	s_setprio 1
	v_mfma_f32_16x16x32_bf16 v[112:115], v[164:167], v[182:185], v[112:115]
	v_mfma_f32_16x16x32_bf16 v[104:107], v[172:175], v[182:185], v[104:107]
	v_mfma_f32_16x16x32_bf16 v[96:99], v[164:167], v[190:193], v[96:99]
	v_mfma_f32_16x16x32_bf16 v[88:91], v[172:175], v[190:193], v[88:91]
	v_mfma_f32_16x16x32_bf16 v[80:83], v[164:167], v[202:205], v[80:83]
	v_mfma_f32_16x16x32_bf16 v[72:75], v[172:175], v[202:205], v[72:75]
	v_mfma_f32_16x16x32_bf16 v[68:71], v[164:167], v[220:223], v[68:71]
	v_mfma_f32_16x16x32_bf16 v[64:67], v[172:175], v[220:223], v[64:67]
	v_mfma_f32_16x16x32_bf16 v[112:115], v[168:171], v[186:189], v[112:115]
	v_mfma_f32_16x16x32_bf16 v[104:107], v[176:179], v[186:189], v[104:107]
	v_mfma_f32_16x16x32_bf16 v[96:99], v[168:171], v[194:197], v[96:99]
	v_mfma_f32_16x16x32_bf16 v[88:91], v[176:179], v[194:197], v[88:91]
	v_mfma_f32_16x16x32_bf16 v[80:83], v[168:171], v[206:209], v[80:83]
	v_mfma_f32_16x16x32_bf16 v[72:75], v[176:179], v[206:209], v[72:75]
	v_mfma_f32_16x16x32_bf16 v[68:71], v[168:171], v[224:227], v[68:71]
	v_mfma_f32_16x16x32_bf16 v[64:67], v[176:179], v[224:227], v[64:67]
	s_setprio 0
	s_barrier
; #define PG8_STAGE(bufoff, gbase, voff) do { _Pragma("unroll") for (int _i = 0; _i < 2; ++_i) \
;         __builtin_amdgcn_global_load_lds((const unsigned*)((const char*)(gbase) + (voff)[_i]), (PG8_LAS unsigned*)(lds + (bufoff) + ldsw + _i * 8192), 16, 0, 0); } while (0)
; #define PG8_STAGE_A(bufoff, gbase, OA, h) do { _Pragma("unroll") for (int _i = 0; _i < 2; ++_i) \
;         __builtin_amdgcn_global_load_lds((const unsigned*)((const char*)(gbase) + (OA)[h][_i]), (PG8_LAS unsigned*)(lds + (bufoff) + ldsw + _i * 8192), 16, 0, 0); } while (0)
; #define PG8_WAIT_V(n) asm volatile("s_waitcnt vmcnt(" #n ")" ::: "memory")
; #define PG8_WAIT_L(n) asm volatile("s_waitcnt lgkmcnt(" #n ")" ::: "memory")
; #define PG8_BAR __builtin_amdgcn_s_barrier()
; #define PG8_SCHED __builtin_amdgcn_sched_barrier(0)
;     ...
;             PG8_LDA(At, 1, 1); PG8_STAGE(PG8_SB(1, 0), b3, voffB); PG8_STAGE(PG8_SB(1, 1), b3 + hstep, voffB); PG8_STAGE_A(PG8_SA(1, 0), a3, o2, 0);
;             PG8_WAIT_V(8); PG8_WAIT_L(0); PG8_BAR; PG8_MMA(1, 0, At, B0); PG8_MMA(1, 1, At, B1); PG8_BAR; PG8_SCHED;
;         }
	s_add_i32 s2, s23, s28
	v_lshl_add_u64 v[142:143], v[142:143], 0, s[92:93]
	s_mov_b32 m0, s2
	ds_read_b128 v[182:185], v146 offset:49152
	ds_read_b128 v[186:189], v146 offset:50176
	ds_read_b128 v[190:193], v146 offset:51200
	ds_read_b128 v[194:197], v146 offset:52224
	ds_read_b128 v[202:205], v146 offset:53248
	ds_read_b128 v[206:209], v146 offset:54272
	ds_read_b128 v[220:223], v146 offset:55296
	ds_read_b128 v[224:227], v146 offset:56320
	global_load_lds_dwordx4 v[142:143], off
	s_add_i32 m0, s2, 0x2000
	s_add_u32 s0, s0, 0x40080
	v_lshl_add_u64 v[142:143], v[198:199], 0, s[92:93]
	s_addc_u32 s1, s1, 0
	s_add_i32 s2, s40, s28
	global_load_lds_dwordx4 v[142:143], off
	s_mov_b32 m0, s2
	s_nop 0
	global_load_lds_dwordx4 v180, s[0:1]
	s_add_i32 m0, s2, 0x2000
	s_nop 0
	global_load_lds_dwordx4 v132, s[0:1]
	v_lshl_add_u64 v[142:143], v[228:229], 0, s[92:93]
	s_mov_b32 m0, s43
	s_nop 0
	global_load_lds_dwordx4 v[142:143], off
	v_lshl_add_u64 v[142:143], v[230:231], 0, s[92:93]
	s_mov_b32 m0, s44
	s_nop 0
	global_load_lds_dwordx4 v[142:143], off
	s_waitcnt vmcnt(8)
	s_waitcnt lgkmcnt(0)
	s_barrier
	s_setprio 1
	s_waitcnt lgkmcnt(0)
	v_mfma_f32_16x16x32_bf16 v[60:63], v[148:151], v[182:185], v[60:63]
	v_mfma_f32_16x16x32_bf16 v[56:59], v[156:159], v[182:185], v[56:59]
	v_mfma_f32_16x16x32_bf16 v[44:47], v[148:151], v[190:193], v[44:47]
	v_mfma_f32_16x16x32_bf16 v[36:39], v[156:159], v[190:193], v[36:39]
	v_mfma_f32_16x16x32_bf16 v[20:23], v[148:151], v[202:205], v[20:23]
	v_mfma_f32_16x16x32_bf16 v[12:15], v[156:159], v[202:205], v[12:15]
	v_mfma_f32_16x16x32_bf16 v[4:7], v[148:151], v[220:223], v[4:7]
	v_mfma_f32_16x16x32_bf16 v[0:3], v[156:159], v[220:223], v[0:3]
	v_mfma_f32_16x16x32_bf16 v[60:63], v[152:155], v[186:189], v[60:63]
	v_mfma_f32_16x16x32_bf16 v[56:59], v[160:163], v[186:189], v[56:59]
	v_mfma_f32_16x16x32_bf16 v[44:47], v[152:155], v[194:197], v[44:47]
	v_mfma_f32_16x16x32_bf16 v[36:39], v[160:163], v[194:197], v[36:39]
	v_mfma_f32_16x16x32_bf16 v[20:23], v[152:155], v[206:209], v[20:23]
	v_mfma_f32_16x16x32_bf16 v[12:15], v[160:163], v[206:209], v[12:15]
	v_mfma_f32_16x16x32_bf16 v[4:7], v[152:155], v[224:227], v[4:7]
	v_mfma_f32_16x16x32_bf16 v[0:3], v[160:163], v[224:227], v[0:3]
	s_setprio 0
	s_setprio 1
	v_mfma_f32_16x16x32_bf16 v[40:43], v[164:167], v[182:185], v[40:43]
	v_mfma_f32_16x16x32_bf16 v[32:35], v[172:175], v[182:185], v[32:35]
	v_mfma_f32_16x16x32_bf16 v[16:19], v[164:167], v[190:193], v[16:19]
	v_mfma_f32_16x16x32_bf16 v[8:11], v[172:175], v[190:193], v[8:11]
	v_mfma_f32_16x16x32_bf16 v[52:55], v[164:167], v[202:205], v[52:55]
	v_mfma_f32_16x16x32_bf16 v[48:51], v[172:175], v[202:205], v[48:51]
	v_mfma_f32_16x16x32_bf16 v[28:31], v[164:167], v[220:223], v[28:31]
	v_mfma_f32_16x16x32_bf16 v[24:27], v[172:175], v[220:223], v[24:27]
	v_mfma_f32_16x16x32_bf16 v[40:43], v[168:171], v[186:189], v[40:43]
	v_mfma_f32_16x16x32_bf16 v[32:35], v[176:179], v[186:189], v[32:35]
	v_mfma_f32_16x16x32_bf16 v[16:19], v[168:171], v[194:197], v[16:19]
	v_mfma_f32_16x16x32_bf16 v[8:11], v[176:179], v[194:197], v[8:11]
	v_mfma_f32_16x16x32_bf16 v[52:55], v[168:171], v[206:209], v[52:55]
	v_mfma_f32_16x16x32_bf16 v[48:51], v[176:179], v[206:209], v[48:51]
	v_mfma_f32_16x16x32_bf16 v[28:31], v[168:171], v[224:227], v[28:31]
	v_mfma_f32_16x16x32_bf16 v[24:27], v[176:179], v[224:227], v[24:27]
	s_setprio 0
	s_barrier
	s_add_i32 s21, s21, 2
	s_add_u32 s4, s4, 0x100
	s_addc_u32 s5, s5, 0
	s_add_u32 s14, s14, 0x100
	s_addc_u32 s15, s15, 0
	s_cmp_gt_u32 s21, 13
	s_cbranch_scc0 .LBB0_179
	s_and_b64 vcc, exec, s[18:19]
	s_cbranch_vccz .LBB0_182
	s_barrier

; #define PG8_STAGE(bufoff, gbase, voff) do { _Pragma("unroll") for (int _i = 0; _i < 2; ++_i) \
;         __builtin_amdgcn_global_load_lds((const unsigned*)((const char*)(gbase) + (voff)[_i]), (PG8_LAS unsigned*)(lds + (bufoff) + ldsw + _i * 8192), 16, 0, 0); } while (0)
; #define PG8_STAGE_A(bufoff, gbase, OA, h) do { _Pragma("unroll") for (int _i = 0; _i < 2; ++_i) \
;         __builtin_amdgcn_global_load_lds((const unsigned*)((const char*)(gbase) + (OA)[h][_i]), (PG8_LAS unsigned*)(lds + (bufoff) + ldsw + _i * 8192), 16, 0, 0); } while (0)
; #define PG8_WAIT_V(n) asm volatile("s_waitcnt vmcnt(" #n ")" ::: "memory")
; #define PG8_WAIT_L(n) asm volatile("s_waitcnt lgkmcnt(" #n ")" ::: "memory")
; #define PG8_BAR __builtin_amdgcn_s_barrier()
; #define PG8_SCHED __builtin_amdgcn_sched_barrier(0)
;     ...
;             PG8_LDB(B0, 0, 0); PG8_LDB(B1, 0, 1); PG8_SCHED; PG8_LDA(At, 0, 0); PG8_STAGE_A(PG8_SA(1, 1), a1, oc, 1);
;             PG8_WAIT_V(8); PG8_WAIT_L(0); PG8_BAR; PG8_MMA(0, 0, At, B0); PG8_MMA(0, 1, At, B1); PG8_BAR; PG8_SCHED;
;             PG8_LDA(At, 0, 1); PG8_STAGE(PG8_SB(0, 0), b2, voffB); PG8_STAGE(PG8_SB(0, 1), b2 + hstep, voffB); PG8_STAGE_A(PG8_SA(0, 0), a2, o2, 0);
;             PG8_WAIT_V(8); PG8_WAIT_L(0); PG8_BAR; PG8_MMA(1, 0, At, B0); PG8_MMA(1, 1, At, B1); PG8_BAR; PG8_SCHED;
.LBB0_1140:
	v_add_u32_e32 v140, s89, v175
	v_add_u32_e32 v170, s49, v175
	ds_read_b128 v[128:131], v140
	ds_read_b128 v[132:135], v140 offset:1024
	ds_read_b128 v[136:139], v140 offset:2048
	ds_read_b128 v[140:143], v140 offset:3072
	ds_read_b128 v[144:147], v170
	ds_read_b128 v[148:151], v170 offset:1024
	ds_read_b128 v[166:169], v170 offset:2048
	ds_read_b128 v[170:173], v170 offset:3072
	s_add_u32 s0, s14, 0x80
	s_addc_u32 s1, s15, 0
	s_cmp_eq_u32 s43, 12
	s_cselect_b32 s3, s47, s1
	s_cselect_b32 s2, s46, s0
	s_cselect_b32 s1, s41, s5
	s_cselect_b32 s0, s40, s4
	s_add_i32 m0, s55, 0xc000
	ds_read_b128 v[182:185], v176
	ds_read_b128 v[186:189], v176 offset:1024
	ds_read_b128 v[190:193], v176 offset:2048
	ds_read_b128 v[194:197], v176 offset:3072
	ds_read_b128 v[202:205], v176 offset:4096
	ds_read_b128 v[206:209], v176 offset:5120
	ds_read_b128 v[220:223], v176 offset:6144
	ds_read_b128 v[224:227], v176 offset:7168
	global_load_lds_dwordx4 v164, s[14:15]
	s_add_i32 m0, s55, 0xe000
	s_nop 0
	global_load_lds_dwordx4 v162, s[14:15]
	s_waitcnt vmcnt(8)
	s_waitcnt lgkmcnt(0)
	s_barrier
	s_setprio 1
	s_waitcnt lgkmcnt(0)
	v_mfma_f32_16x16x32_bf16 v[124:127], v[128:131], v[182:185], v[124:127]
	v_mfma_f32_16x16x32_bf16 v[120:123], v[136:139], v[182:185], v[120:123]
	v_mfma_f32_16x16x32_bf16 v[108:111], v[128:131], v[190:193], v[108:111]
	v_mfma_f32_16x16x32_bf16 v[104:107], v[136:139], v[190:193], v[104:107]
	v_mfma_f32_16x16x32_bf16 v[92:95], v[128:131], v[202:205], v[92:95]
	v_mfma_f32_16x16x32_bf16 v[88:91], v[136:139], v[202:205], v[88:91]
	v_mfma_f32_16x16x32_bf16 v[76:79], v[128:131], v[220:223], v[76:79]
	v_mfma_f32_16x16x32_bf16 v[72:75], v[136:139], v[220:223], v[72:75]
	v_mfma_f32_16x16x32_bf16 v[124:127], v[132:135], v[186:189], v[124:127]
	v_mfma_f32_16x16x32_bf16 v[120:123], v[140:143], v[186:189], v[120:123]
	v_mfma_f32_16x16x32_bf16 v[108:111], v[132:135], v[194:197], v[108:111]
	v_mfma_f32_16x16x32_bf16 v[104:107], v[140:143], v[194:197], v[104:107]
	v_mfma_f32_16x16x32_bf16 v[92:95], v[132:135], v[206:209], v[92:95]
	v_mfma_f32_16x16x32_bf16 v[88:91], v[140:143], v[206:209], v[88:91]
	v_mfma_f32_16x16x32_bf16 v[76:79], v[132:135], v[224:227], v[76:79]
	v_mfma_f32_16x16x32_bf16 v[72:75], v[140:143], v[224:227], v[72:75]
	s_setprio 0
	s_setprio 1
	v_mfma_f32_16x16x32_bf16 v[116:119], v[144:147], v[182:185], v[116:119]
	v_mfma_f32_16x16x32_bf16 v[112:115], v[166:169], v[182:185], v[112:115]
	v_mfma_f32_16x16x32_bf16 v[100:103], v[144:147], v[190:193], v[100:103]
	v_mfma_f32_16x16x32_bf16 v[96:99], v[166:169], v[190:193], v[96:99]
	v_mfma_f32_16x16x32_bf16 v[84:87], v[144:147], v[202:205], v[84:87]
	v_mfma_f32_16x16x32_bf16 v[80:83], v[166:169], v[202:205], v[80:83]
	v_mfma_f32_16x16x32_bf16 v[68:71], v[144:147], v[220:223], v[68:71]
	v_mfma_f32_16x16x32_bf16 v[64:67], v[166:169], v[220:223], v[64:67]
	v_mfma_f32_16x16x32_bf16 v[116:119], v[148:151], v[186:189], v[116:119]
	v_mfma_f32_16x16x32_bf16 v[112:115], v[170:173], v[186:189], v[112:115]
	v_mfma_f32_16x16x32_bf16 v[100:103], v[148:151], v[194:197], v[100:103]
	v_mfma_f32_16x16x32_bf16 v[96:99], v[170:173], v[194:197], v[96:99]
	v_mfma_f32_16x16x32_bf16 v[84:87], v[148:151], v[206:209], v[84:87]
	v_mfma_f32_16x16x32_bf16 v[80:83], v[170:173], v[206:209], v[80:83]
	v_mfma_f32_16x16x32_bf16 v[68:71], v[148:151], v[224:227], v[68:71]
	v_mfma_f32_16x16x32_bf16 v[64:67], v[170:173], v[224:227], v[64:67]
	s_setprio 0
	s_barrier
	s_add_i32 s45, s89, s19
	v_lshl_add_u64 v[178:179], s[0:1], 0, v[180:181]
	s_mov_b32 m0, s45
	ds_read_b128 v[182:185], v176 offset:16384
	ds_read_b128 v[186:189], v176 offset:17408
	ds_read_b128 v[190:193], v176 offset:18432
	ds_read_b128 v[194:197], v176 offset:19456
	ds_read_b128 v[202:205], v176 offset:20480
	ds_read_b128 v[206:209], v176 offset:21504
	ds_read_b128 v[220:223], v176 offset:22528
	ds_read_b128 v[224:227], v176 offset:23552
	global_load_lds_dwordx4 v180, s[0:1]
	s_add_i32 m0, s45, 0x2000
	s_add_u32 s62, s0, 0x40000
	v_lshl_add_u64 v[198:199], s[0:1], 0, v[156:157]
	s_addc_u32 s63, s1, 0
	s_add_i32 s45, s49, s19
	global_load_lds_dwordx4 v156, s[0:1]
	s_mov_b32 m0, s45
	v_lshl_add_u64 v[230:231], s[2:3], 0, v[152:153]
	global_load_lds_dwordx4 v180, s[62:63]
	s_add_i32 m0, s45, 0x2000
	s_nop 0
	global_load_lds_dwordx4 v156, s[62:63]
	v_lshl_add_u64 v[228:229], s[2:3], 0, v[158:159]
	s_mov_b32 m0, s55
	s_nop 0
	global_load_lds_dwordx4 v158, s[2:3]
	s_add_i32 m0, s55, 0x2000
	s_nop 0
	global_load_lds_dwordx4 v152, s[2:3]
	s_waitcnt vmcnt(8)
	s_waitcnt lgkmcnt(0)
	s_barrier
; #define PG8_STAGE(bufoff, gbase, voff) do { _Pragma("unroll") for (int _i = 0; _i < 2; ++_i) \
;         __builtin_amdgcn_global_load_lds((const unsigned*)((const char*)(gbase) + (voff)[_i]), (PG8_LAS unsigned*)(lds + (bufoff) + ldsw + _i * 8192), 16, 0, 0); } while (0)
; #define PG8_STAGE_A(bufoff, gbase, OA, h) do { _Pragma("unroll") for (int _i = 0; _i < 2; ++_i) \
;         __builtin_amdgcn_global_load_lds((const unsigned*)((const char*)(gbase) + (OA)[h][_i]), (PG8_LAS unsigned*)(lds + (bufoff) + ldsw + _i * 8192), 16, 0, 0); } while (0)
; #define PG8_WAIT_V(n) asm volatile("s_waitcnt vmcnt(" #n ")" ::: "memory")
; #define PG8_WAIT_L(n) asm volatile("s_waitcnt lgkmcnt(" #n ")" ::: "memory")
; #define PG8_BAR __builtin_amdgcn_s_barrier()
; #define PG8_SCHED __builtin_amdgcn_sched_barrier(0)
;     ...
;             PG8_WAIT_V(8); PG8_WAIT_L(0); PG8_BAR; PG8_MMA(0, 0, At, B0); PG8_MMA(0, 1, At, B1); PG8_BAR; PG8_SCHED;
;             PG8_LDA(At, 0, 1); PG8_STAGE(PG8_SB(0, 0), b2, voffB); PG8_STAGE(PG8_SB(0, 1), b2 + hstep, voffB); PG8_STAGE_A(PG8_SA(0, 0), a2, o2, 0);
;             PG8_WAIT_V(8); PG8_WAIT_L(0); PG8_BAR; PG8_MMA(1, 0, At, B0); PG8_MMA(1, 1, At, B1); PG8_BAR; PG8_SCHED;
;             PG8_LDB(B0, 1, 0); PG8_LDB(B1, 1, 1); PG8_SCHED; PG8_LDA(At, 1, 0); PG8_STAGE_A(PG8_SA(0, 1), a2, o2, 1);
;             PG8_WAIT_V(8); PG8_WAIT_L(0); PG8_BAR; PG8_MMA(0, 0, At, B0); PG8_MMA(0, 1, At, B1); PG8_BAR; PG8_SCHED;
	s_setprio 1
	s_waitcnt lgkmcnt(0)
	v_mfma_f32_16x16x32_bf16 v[60:63], v[128:131], v[182:185], v[60:63]
	v_mfma_f32_16x16x32_bf16 v[56:59], v[136:139], v[182:185], v[56:59]
	v_mfma_f32_16x16x32_bf16 v[44:47], v[128:131], v[190:193], v[44:47]
	v_mfma_f32_16x16x32_bf16 v[40:43], v[136:139], v[190:193], v[40:43]
	v_mfma_f32_16x16x32_bf16 v[20:23], v[128:131], v[202:205], v[20:23]
	v_mfma_f32_16x16x32_bf16 v[16:19], v[136:139], v[202:205], v[16:19]
	v_mfma_f32_16x16x32_bf16 v[4:7], v[128:131], v[220:223], v[4:7]
	v_mfma_f32_16x16x32_bf16 v[0:3], v[136:139], v[220:223], v[0:3]
	v_mfma_f32_16x16x32_bf16 v[60:63], v[132:135], v[186:189], v[60:63]
	v_mfma_f32_16x16x32_bf16 v[56:59], v[140:143], v[186:189], v[56:59]
	v_mfma_f32_16x16x32_bf16 v[44:47], v[132:135], v[194:197], v[44:47]
	v_mfma_f32_16x16x32_bf16 v[40:43], v[140:143], v[194:197], v[40:43]
	v_mfma_f32_16x16x32_bf16 v[20:23], v[132:135], v[206:209], v[20:23]
	v_mfma_f32_16x16x32_bf16 v[16:19], v[140:143], v[206:209], v[16:19]
	v_mfma_f32_16x16x32_bf16 v[4:7], v[132:135], v[224:227], v[4:7]
	v_mfma_f32_16x16x32_bf16 v[0:3], v[140:143], v[224:227], v[0:3]
	s_setprio 0
	s_setprio 1
	v_mfma_f32_16x16x32_bf16 v[52:55], v[144:147], v[182:185], v[52:55]
	v_mfma_f32_16x16x32_bf16 v[48:51], v[166:169], v[182:185], v[48:51]
	v_mfma_f32_16x16x32_bf16 v[28:31], v[144:147], v[190:193], v[28:31]
	v_mfma_f32_16x16x32_bf16 v[24:27], v[166:169], v[190:193], v[24:27]
	v_mfma_f32_16x16x32_bf16 v[36:39], v[144:147], v[202:205], v[36:39]
	v_mfma_f32_16x16x32_bf16 v[32:35], v[166:169], v[202:205], v[32:35]
	v_mfma_f32_16x16x32_bf16 v[12:15], v[144:147], v[220:223], v[12:15]
	v_mfma_f32_16x16x32_bf16 v[8:11], v[166:169], v[220:223], v[8:11]
	v_mfma_f32_16x16x32_bf16 v[52:55], v[148:151], v[186:189], v[52:55]
	v_mfma_f32_16x16x32_bf16 v[48:51], v[170:173], v[186:189], v[48:51]
	v_mfma_f32_16x16x32_bf16 v[28:31], v[148:151], v[194:197], v[28:31]
	v_mfma_f32_16x16x32_bf16 v[24:27], v[170:173], v[194:197], v[24:27]
	v_mfma_f32_16x16x32_bf16 v[36:39], v[148:151], v[206:209], v[36:39]
	v_mfma_f32_16x16x32_bf16 v[32:35], v[170:173], v[206:209], v[32:35]
	v_mfma_f32_16x16x32_bf16 v[12:15], v[148:151], v[224:227], v[12:15]
	v_mfma_f32_16x16x32_bf16 v[8:11], v[170:173], v[224:227], v[8:11]
	s_setprio 0
	s_barrier
	s_add_i32 s45, 0, 0x18000
	s_add_i32 s61, 0, 0x1c000
	v_add_u32_e32 v140, s45, v175
	v_add_u32_e32 v170, s61, v175
	ds_read_b128 v[128:131], v140
	ds_read_b128 v[132:135], v140 offset:1024
	ds_read_b128 v[136:139], v140 offset:2048
	ds_read_b128 v[140:143], v140 offset:3072
	ds_read_b128 v[144:147], v170
	ds_read_b128 v[148:151], v170 offset:1024
	ds_read_b128 v[166:169], v170 offset:2048
	ds_read_b128 v[170:173], v170 offset:3072
	s_add_i32 m0, s55, 0x4000
	ds_read_b128 v[182:185], v176 offset:32768
	ds_read_b128 v[186:189], v176 offset:33792
	ds_read_b128 v[190:193], v176 offset:34816
	ds_read_b128 v[194:197], v176 offset:35840
	ds_read_b128 v[202:205], v176 offset:36864
	ds_read_b128 v[206:209], v176 offset:37888
	ds_read_b128 v[220:223], v176 offset:38912
	ds_read_b128 v[224:227], v176 offset:39936
	global_load_lds_dwordx4 v160, s[2:3]
	s_add_i32 m0, s55, 0x6000
	s_nop 0
	global_load_lds_dwordx4 v154, s[2:3]
	s_waitcnt vmcnt(8)
	s_waitcnt lgkmcnt(0)
	s_barrier
	s_setprio 1
	s_waitcnt lgkmcnt(0)
	v_mfma_f32_16x16x32_bf16 v[124:127], v[128:131], v[182:185], v[124:127]
	v_mfma_f32_16x16x32_bf16 v[120:123], v[136:139], v[182:185], v[120:123]
	v_mfma_f32_16x16x32_bf16 v[108:111], v[128:131], v[190:193], v[108:111]
	v_mfma_f32_16x16x32_bf16 v[104:107], v[136:139], v[190:193], v[104:107]
	v_mfma_f32_16x16x32_bf16 v[92:95], v[128:131], v[202:205], v[92:95]
	v_mfma_f32_16x16x32_bf16 v[88:91], v[136:139], v[202:205], v[88:91]
	v_mfma_f32_16x16x32_bf16 v[76:79], v[128:131], v[220:223], v[76:79]
	v_mfma_f32_16x16x32_bf16 v[72:75], v[136:139], v[220:223], v[72:75]
	v_mfma_f32_16x16x32_bf16 v[124:127], v[132:135], v[186:189], v[124:127]
	v_mfma_f32_16x16x32_bf16 v[120:123], v[140:143], v[186:189], v[120:123]
	v_mfma_f32_16x16x32_bf16 v[108:111], v[132:135], v[194:197], v[108:111]
	v_mfma_f32_16x16x32_bf16 v[104:107], v[140:143], v[194:197], v[104:107]
	v_mfma_f32_16x16x32_bf16 v[92:95], v[132:135], v[206:209], v[92:95]
	v_mfma_f32_16x16x32_bf16 v[88:91], v[140:143], v[206:209], v[88:91]
	v_mfma_f32_16x16x32_bf16 v[76:79], v[132:135], v[224:227], v[76:79]
	v_mfma_f32_16x16x32_bf16 v[72:75], v[140:143], v[224:227], v[72:75]
	s_setprio 0
	s_setprio 1
	v_mfma_f32_16x16x32_bf16 v[116:119], v[144:147], v[182:185], v[116:119]
	v_mfma_f32_16x16x32_bf16 v[112:115], v[166:169], v[182:185], v[112:115]
	v_mfma_f32_16x16x32_bf16 v[100:103], v[144:147], v[190:193], v[100:103]
	v_mfma_f32_16x16x32_bf16 v[96:99], v[166:169], v[190:193], v[96:99]
	v_mfma_f32_16x16x32_bf16 v[84:87], v[144:147], v[202:205], v[84:87]
	v_mfma_f32_16x16x32_bf16 v[80:83], v[166:169], v[202:205], v[80:83]
	v_mfma_f32_16x16x32_bf16 v[68:71], v[144:147], v[220:223], v[68:71]
	v_mfma_f32_16x16x32_bf16 v[64:67], v[166:169], v[220:223], v[64:67]
	v_mfma_f32_16x16x32_bf16 v[116:119], v[148:151], v[186:189], v[116:119]
	v_mfma_f32_16x16x32_bf16 v[112:115], v[170:173], v[186:189], v[112:115]
	v_mfma_f32_16x16x32_bf16 v[100:103], v[148:151], v[194:197], v[100:103]
	v_mfma_f32_16x16x32_bf16 v[96:99], v[170:173], v[194:197], v[96:99]
	v_mfma_f32_16x16x32_bf16 v[84:87], v[148:151], v[206:209], v[84:87]
	v_mfma_f32_16x16x32_bf16 v[80:83], v[170:173], v[206:209], v[80:83]
	v_mfma_f32_16x16x32_bf16 v[68:71], v[148:151], v[224:227], v[68:71]
	v_mfma_f32_16x16x32_bf16 v[64:67], v[170:173], v[224:227], v[64:67]
	s_setprio 0
	s_barrier
; #define PG8_STAGE(bufoff, gbase, voff) do { _Pragma("unroll") for (int _i = 0; _i < 2; ++_i) \
;         __builtin_amdgcn_global_load_lds((const unsigned*)((const char*)(gbase) + (voff)[_i]), (PG8_LAS unsigned*)(lds + (bufoff) + ldsw + _i * 8192), 16, 0, 0); } while (0)
; #define PG8_STAGE_A(bufoff, gbase, OA, h) do { _Pragma("unroll") for (int _i = 0; _i < 2; ++_i) \
;         __builtin_amdgcn_global_load_lds((const unsigned*)((const char*)(gbase) + (OA)[h][_i]), (PG8_LAS unsigned*)(lds + (bufoff) + ldsw + _i * 8192), 16, 0, 0); } while (0)
; #define PG8_WAIT_V(n) asm volatile("s_waitcnt vmcnt(" #n ")" ::: "memory")
; #define PG8_WAIT_L(n) asm volatile("s_waitcnt lgkmcnt(" #n ")" ::: "memory")
; #define PG8_BAR __builtin_amdgcn_s_barrier()
; #define PG8_SCHED __builtin_amdgcn_sched_barrier(0)
;     ...
;             PG8_LDA(At, 1, 1); PG8_STAGE(PG8_SB(1, 0), b3, voffB); PG8_STAGE(PG8_SB(1, 1), b3 + hstep, voffB); PG8_STAGE_A(PG8_SA(1, 0), a3, o2, 0);
;             PG8_WAIT_V(8); PG8_WAIT_L(0); PG8_BAR; PG8_MMA(1, 0, At, B0); PG8_MMA(1, 1, At, B1); PG8_BAR; PG8_SCHED;
;         }
	s_add_i32 s2, s45, s19
	v_lshl_add_u64 v[178:179], v[178:179], 0, s[92:93]
	s_mov_b32 m0, s2
	ds_read_b128 v[182:185], v176 offset:49152
	ds_read_b128 v[186:189], v176 offset:50176
	ds_read_b128 v[190:193], v176 offset:51200
	ds_read_b128 v[194:197], v176 offset:52224
	ds_read_b128 v[202:205], v176 offset:53248
	ds_read_b128 v[206:209], v176 offset:54272
	ds_read_b128 v[220:223], v176 offset:55296
	ds_read_b128 v[224:227], v176 offset:56320
	global_load_lds_dwordx4 v[178:179], off
	s_add_i32 m0, s2, 0x2000
	s_add_u32 s0, s0, 0x40080
	v_lshl_add_u64 v[178:179], v[198:199], 0, s[92:93]
	s_addc_u32 s1, s1, 0
	s_add_i32 s2, s61, s19
	global_load_lds_dwordx4 v[178:179], off
	s_mov_b32 m0, s2
	s_nop 0
	global_load_lds_dwordx4 v180, s[0:1]
	s_add_i32 m0, s2, 0x2000
	s_nop 0
	global_load_lds_dwordx4 v156, s[0:1]
	v_lshl_add_u64 v[178:179], v[228:229], 0, s[92:93]
	s_mov_b32 m0, s56
	s_nop 0
	global_load_lds_dwordx4 v[178:179], off
	v_lshl_add_u64 v[178:179], v[230:231], 0, s[92:93]
	s_mov_b32 m0, s57
	s_nop 0
	global_load_lds_dwordx4 v[178:179], off
	s_waitcnt vmcnt(8)
	s_waitcnt lgkmcnt(0)
	s_barrier
	s_setprio 1
	s_waitcnt lgkmcnt(0)
	v_mfma_f32_16x16x32_bf16 v[60:63], v[128:131], v[182:185], v[60:63]
	v_mfma_f32_16x16x32_bf16 v[56:59], v[136:139], v[182:185], v[56:59]
	v_mfma_f32_16x16x32_bf16 v[44:47], v[128:131], v[190:193], v[44:47]
	v_mfma_f32_16x16x32_bf16 v[40:43], v[136:139], v[190:193], v[40:43]
	v_mfma_f32_16x16x32_bf16 v[20:23], v[128:131], v[202:205], v[20:23]
	v_mfma_f32_16x16x32_bf16 v[16:19], v[136:139], v[202:205], v[16:19]
	v_mfma_f32_16x16x32_bf16 v[4:7], v[128:131], v[220:223], v[4:7]
	v_mfma_f32_16x16x32_bf16 v[0:3], v[136:139], v[220:223], v[0:3]
	v_mfma_f32_16x16x32_bf16 v[60:63], v[132:135], v[186:189], v[60:63]
	v_mfma_f32_16x16x32_bf16 v[56:59], v[140:143], v[186:189], v[56:59]
	v_mfma_f32_16x16x32_bf16 v[44:47], v[132:135], v[194:197], v[44:47]
	v_mfma_f32_16x16x32_bf16 v[40:43], v[140:143], v[194:197], v[40:43]
	v_mfma_f32_16x16x32_bf16 v[20:23], v[132:135], v[206:209], v[20:23]
	v_mfma_f32_16x16x32_bf16 v[16:19], v[140:143], v[206:209], v[16:19]
	v_mfma_f32_16x16x32_bf16 v[4:7], v[132:135], v[224:227], v[4:7]
	v_mfma_f32_16x16x32_bf16 v[0:3], v[140:143], v[224:227], v[0:3]
	s_setprio 0
	s_setprio 1
	v_mfma_f32_16x16x32_bf16 v[52:55], v[144:147], v[182:185], v[52:55]
	v_mfma_f32_16x16x32_bf16 v[48:51], v[166:169], v[182:185], v[48:51]
	v_mfma_f32_16x16x32_bf16 v[28:31], v[144:147], v[190:193], v[28:31]
	v_mfma_f32_16x16x32_bf16 v[24:27], v[166:169], v[190:193], v[24:27]
	v_mfma_f32_16x16x32_bf16 v[36:39], v[144:147], v[202:205], v[36:39]
	v_mfma_f32_16x16x32_bf16 v[32:35], v[166:169], v[202:205], v[32:35]
	v_mfma_f32_16x16x32_bf16 v[12:15], v[144:147], v[220:223], v[12:15]
	v_mfma_f32_16x16x32_bf16 v[8:11], v[166:169], v[220:223], v[8:11]
	v_mfma_f32_16x16x32_bf16 v[52:55], v[148:151], v[186:189], v[52:55]
	v_mfma_f32_16x16x32_bf16 v[48:51], v[170:173], v[186:189], v[48:51]
	v_mfma_f32_16x16x32_bf16 v[28:31], v[148:151], v[194:197], v[28:31]
	v_mfma_f32_16x16x32_bf16 v[24:27], v[170:173], v[194:197], v[24:27]
	v_mfma_f32_16x16x32_bf16 v[36:39], v[148:151], v[206:209], v[36:39]
	v_mfma_f32_16x16x32_bf16 v[32:35], v[170:173], v[206:209], v[32:35]
	v_mfma_f32_16x16x32_bf16 v[12:15], v[148:151], v[224:227], v[12:15]
	v_mfma_f32_16x16x32_bf16 v[8:11], v[170:173], v[224:227], v[8:11]
	s_setprio 0
	s_barrier
	s_add_i32 s43, s43, 2
	s_add_u32 s4, s4, 0x100
	s_addc_u32 s5, s5, 0
	s_add_u32 s14, s14, 0x100
	s_addc_u32 s15, s15, 0
	s_cmp_gt_u32 s43, 13
	s_cbranch_scc0 .LBB0_1140
	s_and_b64 vcc, exec, s[26:27]
	s_cbranch_vccz .LBB0_1143
	s_barrier

; #define PG8_STAGE(bufoff, gbase, voff) do { _Pragma("unroll") for (int _i = 0; _i < 2; ++_i) \
;         __builtin_amdgcn_global_load_lds((const unsigned*)((const char*)(gbase) + (voff)[_i]), (PG8_LAS unsigned*)(lds + (bufoff) + ldsw + _i * 8192), 16, 0, 0); } while (0)
; #define PG8_STAGE_A(bufoff, gbase, OA, h) do { _Pragma("unroll") for (int _i = 0; _i < 2; ++_i) \
;         __builtin_amdgcn_global_load_lds((const unsigned*)((const char*)(gbase) + (OA)[h][_i]), (PG8_LAS unsigned*)(lds + (bufoff) + ldsw + _i * 8192), 16, 0, 0); } while (0)
; #define PG8_WAIT_V(n) asm volatile("s_waitcnt vmcnt(" #n ")" ::: "memory")
; #define PG8_WAIT_L(n) asm volatile("s_waitcnt lgkmcnt(" #n ")" ::: "memory")
; #define PG8_BAR __builtin_amdgcn_s_barrier()
; #define PG8_SCHED __builtin_amdgcn_sched_barrier(0)
;     ...
;             PG8_LDB(B0, 0, 0); PG8_LDB(B1, 0, 1); PG8_SCHED; PG8_LDA(At, 0, 0); PG8_STAGE_A(PG8_SA(1, 1), a1, oc, 1);
;             PG8_WAIT_V(8); PG8_WAIT_L(0); PG8_BAR; PG8_MMA(0, 0, At, B0); PG8_MMA(0, 1, At, B1); PG8_BAR; PG8_SCHED;
;             PG8_LDA(At, 0, 1); PG8_STAGE(PG8_SB(0, 0), b2, voffB); PG8_STAGE(PG8_SB(0, 1), b2 + hstep, voffB); PG8_STAGE_A(PG8_SA(0, 0), a2, o2, 0);
;             PG8_WAIT_V(8); PG8_WAIT_L(0); PG8_BAR; PG8_MMA(1, 0, At, B0); PG8_MMA(1, 1, At, B1); PG8_BAR; PG8_SCHED;
.LBB0_1603:
	ds_read_b128 v[16:19], v167
	ds_read_b128 v[20:23], v191
	ds_read_b128 v[24:27], v210
	ds_read_b128 v[28:31], v215
	ds_read_b128 v[0:3], v226
	ds_read_b128 v[4:7], v227
	ds_read_b128 v[8:11], v219
	ds_read_b128 v[12:15], v220
	s_add_u32 s2, s9, s74
	s_addc_u32 s3, s12, s75
	s_add_u32 s47, s2, 0x9400100
	s_addc_u32 s52, s3, 0
	s_and_b64 s[2:3], s[0:1], exec
	s_cselect_b32 s3, s21, s52
	s_cselect_b32 s2, s20, s47
	s_add_u32 s47, s25, s74
	s_addc_u32 s52, s45, s75
	s_and_b64 s[0:1], s[0:1], exec
	s_cselect_b32 s1, s27, s52
	s_cselect_b32 s0, s26, s47
	v_lshl_add_u64 v[184:185], v[174:175], 0, s[74:75]
	s_add_i32 m0, s7, 0xc000
	ds_read_b128 v[236:239], v225
	ds_read_b128 v[240:243], v225 offset:16
	ds_read_b128 v[244:247], v225 offset:2048
	ds_read_b128 v[248:251], v225 offset:2064
	ds_read_b128 v[202:205], v225 offset:4096
	ds_read_b128 v[206:209], v225 offset:4112
	ds_read_b128 v[192:195], v225 offset:6144
	ds_read_b128 v[196:199], v225 offset:6160
	global_load_lds_dwordx4 v[184:185], off
	v_lshl_add_u64 v[184:185], v[172:173], 0, s[74:75]
	s_add_i32 m0, s7, 0xe000
	s_nop 0
	global_load_lds_dwordx4 v[184:185], off
	s_waitcnt vmcnt(8)
	s_waitcnt lgkmcnt(0)
	s_barrier
	s_setprio 1
	s_waitcnt lgkmcnt(0)
	v_mfma_scale_f32_16x16x128_f8f6f4 v[156:159], v[16:23], v[236:243], v[156:159], v211, v212 op_sel_hi:[0,0,0]
	v_mfma_scale_f32_16x16x128_f8f6f4 v[152:155], v[24:31], v[236:243], v[152:155], v211, v212 op_sel_hi:[0,0,0]
	v_mfma_scale_f32_16x16x128_f8f6f4 v[140:143], v[16:23], v[244:251], v[140:143], v211, v212 op_sel_hi:[0,0,0]
	v_mfma_scale_f32_16x16x128_f8f6f4 v[132:135], v[24:31], v[244:251], v[132:135], v211, v212 op_sel_hi:[0,0,0]
	v_mfma_scale_f32_16x16x128_f8f6f4 v[124:127], v[16:23], v[202:209], v[124:127], v211, v212 op_sel_hi:[0,0,0]
	v_mfma_scale_f32_16x16x128_f8f6f4 v[120:123], v[24:31], v[202:209], v[120:123], v211, v212 op_sel_hi:[0,0,0]
	v_mfma_scale_f32_16x16x128_f8f6f4 v[108:111], v[16:23], v[192:199], v[108:111], v211, v212 op_sel_hi:[0,0,0]
	v_mfma_scale_f32_16x16x128_f8f6f4 v[100:103], v[24:31], v[192:199], v[100:103], v211, v212 op_sel_hi:[0,0,0]
	s_setprio 0
	s_setprio 1
	v_mfma_scale_f32_16x16x128_f8f6f4 v[148:151], v[0:7], v[236:243], v[148:151], v211, v212 op_sel_hi:[0,0,0]
	v_mfma_scale_f32_16x16x128_f8f6f4 v[144:147], v[8:15], v[236:243], v[144:147], v211, v212 op_sel_hi:[0,0,0]
	v_mfma_scale_f32_16x16x128_f8f6f4 v[136:139], v[0:7], v[244:251], v[136:139], v211, v212 op_sel_hi:[0,0,0]
	v_mfma_scale_f32_16x16x128_f8f6f4 v[128:131], v[8:15], v[244:251], v[128:131], v211, v212 op_sel_hi:[0,0,0]
	v_mfma_scale_f32_16x16x128_f8f6f4 v[116:119], v[0:7], v[202:209], v[116:119], v211, v212 op_sel_hi:[0,0,0]
	v_mfma_scale_f32_16x16x128_f8f6f4 v[112:115], v[8:15], v[202:209], v[112:115], v211, v212 op_sel_hi:[0,0,0]
	v_mfma_scale_f32_16x16x128_f8f6f4 v[104:107], v[0:7], v[192:199], v[104:107], v211, v212 op_sel_hi:[0,0,0]
	v_mfma_scale_f32_16x16x128_f8f6f4 v[96:99], v[8:15], v[192:199], v[96:99], v211, v212 op_sel_hi:[0,0,0]
	s_setprio 0
	s_barrier
	v_lshl_add_u64 v[184:185], s[0:1], 0, v[162:163]
	s_add_i32 m0, s7, 0x10000
	ds_read_b128 v[192:195], v225 offset:16384
	ds_read_b128 v[196:199], v225 offset:16400
	ds_read_b128 v[202:205], v225 offset:18432
	ds_read_b128 v[206:209], v225 offset:18448
	ds_read_b128 v[236:239], v225 offset:20480
	ds_read_b128 v[240:243], v225 offset:20496
	ds_read_b128 v[244:247], v225 offset:22528
	ds_read_b128 v[248:251], v225 offset:22544
	global_load_lds_dwordx4 v162, s[0:1]
	s_add_i32 m0, s7, 0x12000
	s_add_u32 s52, s0, 0x20000
	v_lshl_add_u64 v[186:187], s[0:1], 0, v[160:161]
	s_addc_u32 s53, s1, 0
	global_load_lds_dwordx4 v160, s[0:1]
	s_add_i32 m0, s7, 0x14000
	v_mov_b32_e32 v183, v181
	global_load_lds_dwordx4 v162, s[52:53]
	s_add_i32 m0, s7, 0x16000
	s_nop 0
	global_load_lds_dwordx4 v160, s[52:53]
	s_mov_b32 m0, s7
	v_lshl_add_u64 v[188:189], s[2:3], 0, v[180:181]
	global_load_lds_dwordx4 v180, s[2:3]
	s_add_i32 m0, s7, 0x2000
	s_nop 0
	global_load_lds_dwordx4 v182, s[2:3]
	s_waitcnt vmcnt(8)
	s_waitcnt lgkmcnt(0)
	v_lshl_add_u64 v[182:183], s[2:3], 0, v[182:183]
	s_barrier
	s_setprio 1
	s_waitcnt lgkmcnt(0)
	v_mfma_scale_f32_16x16x128_f8f6f4 v[92:95], v[16:23], v[192:199], v[92:95], v211, v212 op_sel_hi:[0,0,0]
	v_mfma_scale_f32_16x16x128_f8f6f4 v[88:91], v[24:31], v[192:199], v[88:91], v211, v212 op_sel_hi:[0,0,0]
	v_mfma_scale_f32_16x16x128_f8f6f4 v[76:79], v[16:23], v[202:209], v[76:79], v211, v212 op_sel_hi:[0,0,0]
	v_mfma_scale_f32_16x16x128_f8f6f4 v[68:71], v[24:31], v[202:209], v[68:71], v211, v212 op_sel_hi:[0,0,0]
	v_mfma_scale_f32_16x16x128_f8f6f4 v[60:63], v[16:23], v[236:243], v[60:63], v211, v212 op_sel_hi:[0,0,0]
	v_mfma_scale_f32_16x16x128_f8f6f4 v[56:59], v[24:31], v[236:243], v[56:59], v211, v212 op_sel_hi:[0,0,0]
	v_mfma_scale_f32_16x16x128_f8f6f4 v[44:47], v[16:23], v[244:251], v[44:47], v211, v212 op_sel_hi:[0,0,0]
	v_mfma_scale_f32_16x16x128_f8f6f4 v[36:39], v[24:31], v[244:251], v[36:39], v211, v212 op_sel_hi:[0,0,0]
	s_setprio 0
	s_setprio 1
	v_mfma_scale_f32_16x16x128_f8f6f4 v[84:87], v[0:7], v[192:199], v[84:87], v211, v212 op_sel_hi:[0,0,0]
	v_mfma_scale_f32_16x16x128_f8f6f4 v[80:83], v[8:15], v[192:199], v[80:83], v211, v212 op_sel_hi:[0,0,0]
	v_mfma_scale_f32_16x16x128_f8f6f4 v[72:75], v[0:7], v[202:209], v[72:75], v211, v212 op_sel_hi:[0,0,0]
	v_mfma_scale_f32_16x16x128_f8f6f4 v[64:67], v[8:15], v[202:209], v[64:67], v211, v212 op_sel_hi:[0,0,0]
	v_mfma_scale_f32_16x16x128_f8f6f4 v[52:55], v[0:7], v[236:243], v[52:55], v211, v212 op_sel_hi:[0,0,0]
	v_mfma_scale_f32_16x16x128_f8f6f4 v[48:51], v[8:15], v[236:243], v[48:51], v211, v212 op_sel_hi:[0,0,0]
	v_mfma_scale_f32_16x16x128_f8f6f4 v[40:43], v[0:7], v[244:251], v[40:43], v211, v212 op_sel_hi:[0,0,0]
	v_mfma_scale_f32_16x16x128_f8f6f4 v[32:35], v[8:15], v[244:251], v[32:35], v211, v212 op_sel_hi:[0,0,0]
	s_setprio 0
	s_barrier
; #define PG8_STAGE(bufoff, gbase, voff) do { _Pragma("unroll") for (int _i = 0; _i < 2; ++_i) \
;         __builtin_amdgcn_global_load_lds((const unsigned*)((const char*)(gbase) + (voff)[_i]), (PG8_LAS unsigned*)(lds + (bufoff) + ldsw + _i * 8192), 16, 0, 0); } while (0)
; #define PG8_STAGE_A(bufoff, gbase, OA, h) do { _Pragma("unroll") for (int _i = 0; _i < 2; ++_i) \
;         __builtin_amdgcn_global_load_lds((const unsigned*)((const char*)(gbase) + (OA)[h][_i]), (PG8_LAS unsigned*)(lds + (bufoff) + ldsw + _i * 8192), 16, 0, 0); } while (0)
; #define PG8_WAIT_V(n) asm volatile("s_waitcnt vmcnt(" #n ")" ::: "memory")
; #define PG8_WAIT_L(n) asm volatile("s_waitcnt lgkmcnt(" #n ")" ::: "memory")
; #define PG8_BAR __builtin_amdgcn_s_barrier()
; #define PG8_SCHED __builtin_amdgcn_sched_barrier(0)
;     ...
;             PG8_LDB(B0, 1, 0); PG8_LDB(B1, 1, 1); PG8_SCHED; PG8_LDA(At, 1, 0); PG8_STAGE_A(PG8_SA(0, 1), a2, o2, 1);
;             PG8_WAIT_V(8); PG8_WAIT_L(0); PG8_BAR; PG8_MMA(0, 0, At, B0); PG8_MMA(0, 1, At, B1); PG8_BAR; PG8_SCHED;
;             PG8_LDA(At, 1, 1); PG8_STAGE(PG8_SB(1, 0), b3, voffB); PG8_STAGE(PG8_SB(1, 1), b3 + hstep, voffB); PG8_STAGE_A(PG8_SA(1, 0), a3, o2, 0);
;             PG8_WAIT_V(8); PG8_WAIT_L(0); PG8_BAR; PG8_MMA(1, 0, At, B0); PG8_MMA(1, 1, At, B1); PG8_BAR; PG8_SCHED;
;         }
	ds_read_b128 v[0:3], v228
	ds_read_b128 v[4:7], v229
	ds_read_b128 v[8:11], v221
	ds_read_b128 v[12:15], v222
	ds_read_b128 v[16:19], v230
	ds_read_b128 v[20:23], v231
	ds_read_b128 v[24:27], v223
	ds_read_b128 v[28:31], v224
	v_lshl_add_u64 v[178:179], s[2:3], 0, v[178:179]
	s_add_i32 m0, s7, 0x4000
	ds_read_b128 v[192:195], v225 offset:32768
	ds_read_b128 v[196:199], v225 offset:32784
	ds_read_b128 v[202:205], v225 offset:34816
	ds_read_b128 v[206:209], v225 offset:34832
	ds_read_b128 v[236:239], v225 offset:36864
	ds_read_b128 v[240:243], v225 offset:36880
	ds_read_b128 v[244:247], v225 offset:38912
	ds_read_b128 v[248:251], v225 offset:38928
	global_load_lds_dwordx4 v[178:179], off
	v_lshl_add_u64 v[176:177], s[2:3], 0, v[176:177]
	s_add_i32 m0, s7, 0x6000
	s_nop 0
	global_load_lds_dwordx4 v[176:177], off
	s_waitcnt vmcnt(8)
	s_waitcnt lgkmcnt(0)
	s_barrier
	s_setprio 1
	s_waitcnt lgkmcnt(0)
	v_mfma_scale_f32_16x16x128_f8f6f4 v[156:159], v[0:7], v[192:199], v[156:159], v211, v212 op_sel_hi:[0,0,0]
	v_mfma_scale_f32_16x16x128_f8f6f4 v[152:155], v[8:15], v[192:199], v[152:155], v211, v212 op_sel_hi:[0,0,0]
	v_mfma_scale_f32_16x16x128_f8f6f4 v[140:143], v[0:7], v[202:209], v[140:143], v211, v212 op_sel_hi:[0,0,0]
	v_mfma_scale_f32_16x16x128_f8f6f4 v[132:135], v[8:15], v[202:209], v[132:135], v211, v212 op_sel_hi:[0,0,0]
	v_mfma_scale_f32_16x16x128_f8f6f4 v[124:127], v[0:7], v[236:243], v[124:127], v211, v212 op_sel_hi:[0,0,0]
	v_mfma_scale_f32_16x16x128_f8f6f4 v[120:123], v[8:15], v[236:243], v[120:123], v211, v212 op_sel_hi:[0,0,0]
	v_mfma_scale_f32_16x16x128_f8f6f4 v[108:111], v[0:7], v[244:251], v[108:111], v211, v212 op_sel_hi:[0,0,0]
	v_mfma_scale_f32_16x16x128_f8f6f4 v[100:103], v[8:15], v[244:251], v[100:103], v211, v212 op_sel_hi:[0,0,0]
	s_setprio 0
	s_setprio 1
	v_mfma_scale_f32_16x16x128_f8f6f4 v[148:151], v[16:23], v[192:199], v[148:151], v211, v212 op_sel_hi:[0,0,0]
	v_mfma_scale_f32_16x16x128_f8f6f4 v[144:147], v[24:31], v[192:199], v[144:147], v211, v212 op_sel_hi:[0,0,0]
	v_mfma_scale_f32_16x16x128_f8f6f4 v[136:139], v[16:23], v[202:209], v[136:139], v211, v212 op_sel_hi:[0,0,0]
	v_mfma_scale_f32_16x16x128_f8f6f4 v[128:131], v[24:31], v[202:209], v[128:131], v211, v212 op_sel_hi:[0,0,0]
	v_mfma_scale_f32_16x16x128_f8f6f4 v[116:119], v[16:23], v[236:243], v[116:119], v211, v212 op_sel_hi:[0,0,0]
	v_mfma_scale_f32_16x16x128_f8f6f4 v[112:115], v[24:31], v[236:243], v[112:115], v211, v212 op_sel_hi:[0,0,0]
	v_mfma_scale_f32_16x16x128_f8f6f4 v[104:107], v[16:23], v[244:251], v[104:107], v211, v212 op_sel_hi:[0,0,0]
	v_mfma_scale_f32_16x16x128_f8f6f4 v[96:99], v[24:31], v[244:251], v[96:99], v211, v212 op_sel_hi:[0,0,0]
	s_setprio 0
	s_barrier
	s_mov_b32 m0, s13
	v_lshl_add_u64 v[176:177], v[184:185], 0, s[92:93]
	s_add_u32 s0, s0, 0x20080
	ds_read_b128 v[192:195], v225 offset:49152
	ds_read_b128 v[196:199], v225 offset:49168
	ds_read_b128 v[202:205], v225 offset:51200
	ds_read_b128 v[206:209], v225 offset:51216
	ds_read_b128 v[236:239], v225 offset:53248
	ds_read_b128 v[240:243], v225 offset:53264
	ds_read_b128 v[244:247], v225 offset:55296
	ds_read_b128 v[248:251], v225 offset:55312
	global_load_lds_dwordx4 v[176:177], off
	v_lshl_add_u64 v[176:177], v[186:187], 0, s[92:93]
	s_mov_b32 m0, s14
	s_addc_u32 s1, s1, 0
	global_load_lds_dwordx4 v[176:177], off
	s_mov_b32 m0, s17
	s_nop 0
	global_load_lds_dwordx4 v162, s[0:1]
	s_mov_b32 m0, s18
	s_nop 0
	global_load_lds_dwordx4 v160, s[0:1]
	v_lshl_add_u64 v[176:177], v[188:189], 0, s[92:93]
	s_mov_b32 m0, s15
	s_nop 0
	global_load_lds_dwordx4 v[176:177], off
	v_lshl_add_u64 v[176:177], v[182:183], 0, s[92:93]
	s_mov_b32 m0, s16
	s_nop 0
	global_load_lds_dwordx4 v[176:177], off
	s_waitcnt vmcnt(8)
	s_waitcnt lgkmcnt(0)
	s_barrier
	s_setprio 1
	s_waitcnt lgkmcnt(0)
	v_mfma_scale_f32_16x16x128_f8f6f4 v[92:95], v[0:7], v[192:199], v[92:95], v211, v212 op_sel_hi:[0,0,0]
	v_mfma_scale_f32_16x16x128_f8f6f4 v[88:91], v[8:15], v[192:199], v[88:91], v211, v212 op_sel_hi:[0,0,0]
	v_mfma_scale_f32_16x16x128_f8f6f4 v[76:79], v[0:7], v[202:209], v[76:79], v211, v212 op_sel_hi:[0,0,0]
	v_mfma_scale_f32_16x16x128_f8f6f4 v[68:71], v[8:15], v[202:209], v[68:71], v211, v212 op_sel_hi:[0,0,0]
	v_mfma_scale_f32_16x16x128_f8f6f4 v[60:63], v[0:7], v[236:243], v[60:63], v211, v212 op_sel_hi:[0,0,0]
	v_mfma_scale_f32_16x16x128_f8f6f4 v[56:59], v[8:15], v[236:243], v[56:59], v211, v212 op_sel_hi:[0,0,0]
	v_mfma_scale_f32_16x16x128_f8f6f4 v[44:47], v[0:7], v[244:251], v[44:47], v211, v212 op_sel_hi:[0,0,0]
	v_mfma_scale_f32_16x16x128_f8f6f4 v[36:39], v[8:15], v[244:251], v[36:39], v211, v212 op_sel_hi:[0,0,0]
	s_setprio 0
	s_setprio 1
	v_mfma_scale_f32_16x16x128_f8f6f4 v[84:87], v[16:23], v[192:199], v[84:87], v211, v212 op_sel_hi:[0,0,0]
	v_mfma_scale_f32_16x16x128_f8f6f4 v[80:83], v[24:31], v[192:199], v[80:83], v211, v212 op_sel_hi:[0,0,0]
	v_mfma_scale_f32_16x16x128_f8f6f4 v[72:75], v[16:23], v[202:209], v[72:75], v211, v212 op_sel_hi:[0,0,0]
	v_mfma_scale_f32_16x16x128_f8f6f4 v[64:67], v[24:31], v[202:209], v[64:67], v211, v212 op_sel_hi:[0,0,0]
	v_mfma_scale_f32_16x16x128_f8f6f4 v[52:55], v[16:23], v[236:243], v[52:55], v211, v212 op_sel_hi:[0,0,0]
	v_mfma_scale_f32_16x16x128_f8f6f4 v[48:51], v[24:31], v[236:243], v[48:51], v211, v212 op_sel_hi:[0,0,0]
	v_mfma_scale_f32_16x16x128_f8f6f4 v[40:43], v[16:23], v[244:251], v[40:43], v211, v212 op_sel_hi:[0,0,0]
	v_mfma_scale_f32_16x16x128_f8f6f4 v[32:35], v[24:31], v[244:251], v[32:35], v211, v212 op_sel_hi:[0,0,0]
	s_setprio 0
	s_barrier
	s_add_i32 s46, s46, 2
	s_add_u32 s74, s74, 0x100
	s_addc_u32 s75, s75, 0
	s_cmp_gt_u32 s46, 5
	s_cbranch_scc1 .LBB0_1606

; #define PG8_STAGE(bufoff, gbase, voff) do { _Pragma("unroll") for (int _i = 0; _i < 2; ++_i) \
;         __builtin_amdgcn_global_load_lds((const unsigned*)((const char*)(gbase) + (voff)[_i]), (PG8_LAS unsigned*)(lds + (bufoff) + ldsw + _i * 8192), 16, 0, 0); } while (0)
; #define PG8_STAGE_A(bufoff, gbase, OA, h) do { _Pragma("unroll") for (int _i = 0; _i < 2; ++_i) \
;         __builtin_amdgcn_global_load_lds((const unsigned*)((const char*)(gbase) + (OA)[h][_i]), (PG8_LAS unsigned*)(lds + (bufoff) + ldsw + _i * 8192), 16, 0, 0); } while (0)
; #define PG8_WAIT_V(n) asm volatile("s_waitcnt vmcnt(" #n ")" ::: "memory")
; #define PG8_WAIT_L(n) asm volatile("s_waitcnt lgkmcnt(" #n ")" ::: "memory")
; #define PG8_BAR __builtin_amdgcn_s_barrier()
; #define PG8_SCHED __builtin_amdgcn_sched_barrier(0)
;     ...
;             PG8_LDB(B0, 0, 0); PG8_LDB(B1, 0, 1); PG8_SCHED; PG8_LDA(At, 0, 0); PG8_STAGE_A(PG8_SA(1, 1), a1, oc, 1);
;             PG8_WAIT_V(8); PG8_WAIT_L(0); PG8_BAR; PG8_MMA(0, 0, At, B0); PG8_MMA(0, 1, At, B1); PG8_BAR; PG8_SCHED;
;             PG8_LDA(At, 0, 1); PG8_STAGE(PG8_SB(0, 0), b2, voffB); PG8_STAGE(PG8_SB(0, 1), b2 + hstep, voffB); PG8_STAGE_A(PG8_SA(0, 0), a2, o2, 0);
;             PG8_WAIT_V(8); PG8_WAIT_L(0); PG8_BAR; PG8_MMA(1, 0, At, B0); PG8_MMA(1, 1, At, B1); PG8_BAR; PG8_SCHED;
.LBB0_1631:
	ds_read_b128 v[24:27], v141
	ds_read_b128 v[28:31], v142
	ds_read_b128 v[56:59], v149
	ds_read_b128 v[60:63], v150
	ds_read_b128 v[158:161], v143
	ds_read_b128 v[162:165], v144
	ds_read_b128 v[166:169], v151
	ds_read_b128 v[170:173], v152
	s_add_u32 s2, s20, 0x8000
	s_addc_u32 s3, s21, 0
	v_lshl_add_u64 v[0:1], s[0:1], 0, v[136:137]
	v_lshl_add_u64 v[0:1], v[0:1], 0, s[92:93]
	s_add_i32 m0, s17, 0xc000
	ds_read_b128 v[4:7], v157
	ds_read_b128 v[8:11], v157 offset:16
	ds_read_b128 v[12:15], v157 offset:2048
	ds_read_b128 v[16:19], v157 offset:2064
	ds_read_b128 v[40:43], v157 offset:4096
	ds_read_b128 v[44:47], v157 offset:4112
	ds_read_b128 v[72:75], v157 offset:6144
	ds_read_b128 v[76:79], v157 offset:6160
	global_load_lds_dwordx4 v[0:1], off
	v_lshl_add_u64 v[0:1], s[0:1], 0, v[130:131]
	v_lshl_add_u64 v[0:1], v[0:1], 0, s[92:93]
	s_add_i32 m0, s17, 0xe000
	s_nop 0
	global_load_lds_dwordx4 v[0:1], off
	s_waitcnt vmcnt(16)
	s_waitcnt lgkmcnt(0)
	s_barrier
	s_setprio 1
	s_waitcnt lgkmcnt(0)
	v_mfma_scale_f32_16x16x128_f8f6f4 v[116:119], v[24:31], v[4:11], 0, v211, v212 op_sel_hi:[0,0,0]
	v_mfma_scale_f32_16x16x128_f8f6f4 v[112:115], v[56:63], v[4:11], 0, v211, v212 op_sel_hi:[0,0,0]
	v_mfma_scale_f32_16x16x128_f8f6f4 v[100:103], v[24:31], v[12:19], 0, v211, v212 op_sel_hi:[0,0,0]
	v_mfma_scale_f32_16x16x128_f8f6f4 v[96:99], v[56:63], v[12:19], 0, v211, v212 op_sel_hi:[0,0,0]
	v_mfma_scale_f32_16x16x128_f8f6f4 v[68:71], v[24:31], v[40:47], 0, v211, v212 op_sel_hi:[0,0,0]
	v_mfma_scale_f32_16x16x128_f8f6f4 v[64:67], v[56:63], v[40:47], 0, v211, v212 op_sel_hi:[0,0,0]
	v_mfma_scale_f32_16x16x128_f8f6f4 v[36:39], v[24:31], v[72:79], 0, v211, v212 op_sel_hi:[0,0,0]
	v_mfma_scale_f32_16x16x128_f8f6f4 v[32:35], v[56:63], v[72:79], 0, v211, v212 op_sel_hi:[0,0,0]
	s_setprio 0
	s_setprio 1
	v_mfma_scale_f32_16x16x128_f8f6f4 v[124:127], v[158:165], v[4:11], 0, v211, v212 op_sel_hi:[0,0,0]
	v_mfma_scale_f32_16x16x128_f8f6f4 v[120:123], v[166:173], v[4:11], 0, v211, v212 op_sel_hi:[0,0,0]
	v_mfma_scale_f32_16x16x128_f8f6f4 v[108:111], v[158:165], v[12:19], 0, v211, v212 op_sel_hi:[0,0,0]
	v_mfma_scale_f32_16x16x128_f8f6f4 v[104:107], v[166:173], v[12:19], 0, v211, v212 op_sel_hi:[0,0,0]
	v_mfma_scale_f32_16x16x128_f8f6f4 v[84:87], v[158:165], v[40:47], 0, v211, v212 op_sel_hi:[0,0,0]
	v_mfma_scale_f32_16x16x128_f8f6f4 v[80:83], v[166:173], v[40:47], 0, v211, v212 op_sel_hi:[0,0,0]
	v_mfma_scale_f32_16x16x128_f8f6f4 v[52:55], v[158:165], v[72:79], 0, v211, v212 op_sel_hi:[0,0,0]
	v_mfma_scale_f32_16x16x128_f8f6f4 v[48:51], v[166:173], v[72:79], 0, v211, v212 op_sel_hi:[0,0,0]
	s_setprio 0
	s_barrier
	v_lshl_add_u64 v[138:139], s[20:21], 0, v[180:181]
	s_add_i32 m0, s17, 0x10000
	ds_read_b128 v[182:185], v157 offset:16384
	ds_read_b128 v[186:189], v157 offset:16400
	ds_read_b128 v[190:193], v157 offset:18432
	ds_read_b128 v[194:197], v157 offset:18448
	ds_read_b128 v[202:205], v157 offset:20480
	ds_read_b128 v[206:209], v157 offset:20496
	ds_read_b128 v[220:223], v157 offset:22528
	ds_read_b128 v[224:227], v157 offset:22544
	global_load_lds_dwordx4 v180, s[20:21]
	v_lshl_add_u64 v[174:175], s[20:21], 0, v[132:133]
	s_add_i32 m0, s17, 0x12000
	s_nop 0
	global_load_lds_dwordx4 v132, s[20:21]
	s_add_i32 m0, s17, 0x14000
	v_lshl_add_u64 v[176:177], s[36:37], 0, v[134:135]
	global_load_lds_dwordx4 v180, s[2:3]
	s_add_i32 m0, s17, 0x16000
	v_lshl_add_u64 v[178:179], s[36:37], 0, v[128:129]
	global_load_lds_dwordx4 v132, s[2:3]
	s_mov_b32 m0, s17
	s_nop 0
	global_load_lds_dwordx4 v134, s[36:37]
	s_add_i32 m0, s17, 0x2000
	s_nop 0
	global_load_lds_dwordx4 v128, s[36:37]
	s_waitcnt vmcnt(16)
	s_waitcnt lgkmcnt(0)
	s_barrier
	s_setprio 1
	s_waitcnt lgkmcnt(0)
	v_mfma_scale_f32_16x16x128_f8f6f4 v[76:79], v[24:31], v[182:189], 0, v211, v212 op_sel_hi:[0,0,0]
	v_mfma_scale_f32_16x16x128_f8f6f4 v[72:75], v[56:63], v[182:189], 0, v211, v212 op_sel_hi:[0,0,0]
	v_mfma_scale_f32_16x16x128_f8f6f4 v[44:47], v[24:31], v[190:197], 0, v211, v212 op_sel_hi:[0,0,0]
	v_mfma_scale_f32_16x16x128_f8f6f4 v[40:43], v[56:63], v[190:197], 0, v211, v212 op_sel_hi:[0,0,0]
	v_mfma_scale_f32_16x16x128_f8f6f4 v[20:23], v[24:31], v[202:209], 0, v211, v212 op_sel_hi:[0,0,0]
	v_mfma_scale_f32_16x16x128_f8f6f4 v[16:19], v[56:63], v[202:209], 0, v211, v212 op_sel_hi:[0,0,0]
	v_mfma_scale_f32_16x16x128_f8f6f4 v[8:11], v[24:31], v[220:227], 0, v211, v212 op_sel_hi:[0,0,0]
	v_mfma_scale_f32_16x16x128_f8f6f4 v[4:7], v[56:63], v[220:227], 0, v211, v212 op_sel_hi:[0,0,0]
	s_setprio 0
	s_setprio 1
	v_mfma_scale_f32_16x16x128_f8f6f4 v[92:95], v[158:165], v[182:189], 0, v211, v212 op_sel_hi:[0,0,0]
	v_mfma_scale_f32_16x16x128_f8f6f4 v[88:91], v[166:173], v[182:189], 0, v211, v212 op_sel_hi:[0,0,0]
	v_mfma_scale_f32_16x16x128_f8f6f4 v[60:63], v[158:165], v[190:197], 0, v211, v212 op_sel_hi:[0,0,0]
	v_mfma_scale_f32_16x16x128_f8f6f4 v[56:59], v[166:173], v[190:197], 0, v211, v212 op_sel_hi:[0,0,0]
	v_mfma_scale_f32_16x16x128_f8f6f4 v[28:31], v[158:165], v[202:209], 0, v211, v212 op_sel_hi:[0,0,0]
	v_mfma_scale_f32_16x16x128_f8f6f4 v[24:27], v[166:173], v[202:209], 0, v211, v212 op_sel_hi:[0,0,0]
	v_mfma_scale_f32_16x16x128_f8f6f4 v[12:15], v[158:165], v[220:227], 0, v211, v212 op_sel_hi:[0,0,0]
	v_mfma_scale_f32_16x16x128_f8f6f4 v[0:3], v[166:173], v[220:227], 0, v211, v212 op_sel_hi:[0,0,0]
	s_setprio 0
	s_barrier
; #define PG8_STAGE(bufoff, gbase, voff) do { _Pragma("unroll") for (int _i = 0; _i < 2; ++_i) \
;         __builtin_amdgcn_global_load_lds((const unsigned*)((const char*)(gbase) + (voff)[_i]), (PG8_LAS unsigned*)(lds + (bufoff) + ldsw + _i * 8192), 16, 0, 0); } while (0)
; #define PG8_STAGE_A(bufoff, gbase, OA, h) do { _Pragma("unroll") for (int _i = 0; _i < 2; ++_i) \
;         __builtin_amdgcn_global_load_lds((const unsigned*)((const char*)(gbase) + (OA)[h][_i]), (PG8_LAS unsigned*)(lds + (bufoff) + ldsw + _i * 8192), 16, 0, 0); } while (0)
; #define PG8_WAIT_V(n) asm volatile("s_waitcnt vmcnt(" #n ")" ::: "memory")
; #define PG8_WAIT_L(n) asm volatile("s_waitcnt lgkmcnt(" #n ")" ::: "memory")
; #define PG8_BAR __builtin_amdgcn_s_barrier()
; #define PG8_SCHED __builtin_amdgcn_sched_barrier(0)
;     ...
;             PG8_LDB(B0, 1, 0); PG8_LDB(B1, 1, 1); PG8_SCHED; PG8_LDA(At, 1, 0); PG8_STAGE_A(PG8_SA(0, 1), a2, o2, 1);
;             PG8_WAIT_V(8); PG8_WAIT_L(0); PG8_BAR; PG8_MMA(0, 0, At, B0); PG8_MMA(0, 1, At, B1); PG8_BAR; PG8_SCHED;
;             PG8_LDA(At, 1, 1); PG8_STAGE(PG8_SB(1, 0), b3, voffB); PG8_STAGE(PG8_SB(1, 1), b3 + hstep, voffB); PG8_STAGE_A(PG8_SA(1, 0), a3, o2, 0);
;             PG8_WAIT_V(8); PG8_WAIT_L(0); PG8_BAR; PG8_MMA(1, 0, At, B0); PG8_MMA(1, 1, At, B1); PG8_BAR; PG8_SCHED;
	ds_read_b128 v[158:161], v145
	ds_read_b128 v[162:165], v146
	ds_read_b128 v[166:169], v153
	ds_read_b128 v[170:173], v154
	ds_read_b128 v[182:185], v147
	ds_read_b128 v[186:189], v148
	ds_read_b128 v[190:193], v155
	ds_read_b128 v[194:197], v156
	s_add_i32 m0, s17, 0x4000
	ds_read_b128 v[202:205], v157 offset:32768
	ds_read_b128 v[206:209], v157 offset:32784
	ds_read_b128 v[220:223], v157 offset:34816
	ds_read_b128 v[224:227], v157 offset:34832
	ds_read_b128 v[236:239], v157 offset:36864
	ds_read_b128 v[240:243], v157 offset:36880
	ds_read_b128 v[244:247], v157 offset:38912
	ds_read_b128 v[248:251], v157 offset:38928
	global_load_lds_dwordx4 v136, s[36:37]
	s_add_i32 m0, s17, 0x6000
	s_nop 0
	global_load_lds_dwordx4 v130, s[36:37]
	s_waitcnt vmcnt(8)
	s_waitcnt lgkmcnt(0)
	s_barrier
	s_setprio 1
	s_waitcnt lgkmcnt(0)
	v_mfma_scale_f32_16x16x128_f8f6f4 v[116:119], v[158:165], v[202:209], v[116:119], v211, v212 op_sel_hi:[0,0,0]
	v_mfma_scale_f32_16x16x128_f8f6f4 v[112:115], v[166:173], v[202:209], v[112:115], v211, v212 op_sel_hi:[0,0,0]
	v_mfma_scale_f32_16x16x128_f8f6f4 v[100:103], v[158:165], v[220:227], v[100:103], v211, v212 op_sel_hi:[0,0,0]
	v_mfma_scale_f32_16x16x128_f8f6f4 v[96:99], v[166:173], v[220:227], v[96:99], v211, v212 op_sel_hi:[0,0,0]
	v_mfma_scale_f32_16x16x128_f8f6f4 v[68:71], v[158:165], v[236:243], v[68:71], v211, v212 op_sel_hi:[0,0,0]
	v_mfma_scale_f32_16x16x128_f8f6f4 v[64:67], v[166:173], v[236:243], v[64:67], v211, v212 op_sel_hi:[0,0,0]
	v_mfma_scale_f32_16x16x128_f8f6f4 v[36:39], v[158:165], v[244:251], v[36:39], v211, v212 op_sel_hi:[0,0,0]
	v_mfma_scale_f32_16x16x128_f8f6f4 v[32:35], v[166:173], v[244:251], v[32:35], v211, v212 op_sel_hi:[0,0,0]
	s_setprio 0
	s_setprio 1
	v_mfma_scale_f32_16x16x128_f8f6f4 v[124:127], v[182:189], v[202:209], v[124:127], v211, v212 op_sel_hi:[0,0,0]
	v_mfma_scale_f32_16x16x128_f8f6f4 v[120:123], v[190:197], v[202:209], v[120:123], v211, v212 op_sel_hi:[0,0,0]
	v_mfma_scale_f32_16x16x128_f8f6f4 v[108:111], v[182:189], v[220:227], v[108:111], v211, v212 op_sel_hi:[0,0,0]
	v_mfma_scale_f32_16x16x128_f8f6f4 v[104:107], v[190:197], v[220:227], v[104:107], v211, v212 op_sel_hi:[0,0,0]
	v_mfma_scale_f32_16x16x128_f8f6f4 v[84:87], v[182:189], v[236:243], v[84:87], v211, v212 op_sel_hi:[0,0,0]
	v_mfma_scale_f32_16x16x128_f8f6f4 v[80:83], v[190:197], v[236:243], v[80:83], v211, v212 op_sel_hi:[0,0,0]
	v_mfma_scale_f32_16x16x128_f8f6f4 v[52:55], v[182:189], v[244:251], v[52:55], v211, v212 op_sel_hi:[0,0,0]
	v_mfma_scale_f32_16x16x128_f8f6f4 v[48:51], v[190:197], v[244:251], v[48:51], v211, v212 op_sel_hi:[0,0,0]
	s_setprio 0
	s_barrier
	s_mov_b32 m0, s18
	v_lshl_add_u64 v[138:139], v[138:139], 0, s[92:93]
	s_add_u32 s0, s20, 0x8080
	ds_read_b128 v[202:205], v157 offset:49152
	ds_read_b128 v[206:209], v157 offset:49168
	ds_read_b128 v[220:223], v157 offset:51200
	ds_read_b128 v[224:227], v157 offset:51216
	ds_read_b128 v[236:239], v157 offset:53248
	ds_read_b128 v[240:243], v157 offset:53264
	ds_read_b128 v[244:247], v157 offset:55296
	ds_read_b128 v[248:251], v157 offset:55312
	global_load_lds_dwordx4 v[138:139], off
	v_lshl_add_u64 v[138:139], v[174:175], 0, s[92:93]
	s_mov_b32 m0, s19
	s_addc_u32 s1, s21, 0
	global_load_lds_dwordx4 v[138:139], off
	s_mov_b32 m0, s38
	s_nop 0
	global_load_lds_dwordx4 v180, s[0:1]
	s_mov_b32 m0, s39
	s_nop 0
	global_load_lds_dwordx4 v132, s[0:1]
	v_lshl_add_u64 v[138:139], v[176:177], 0, s[92:93]
	s_mov_b32 m0, s28
	s_nop 0
	global_load_lds_dwordx4 v[138:139], off
	v_lshl_add_u64 v[138:139], v[178:179], 0, s[92:93]
	s_mov_b32 m0, s29
	s_nop 0
	global_load_lds_dwordx4 v[138:139], off
	s_waitcnt vmcnt(8)
	s_waitcnt lgkmcnt(0)
	s_barrier
	s_setprio 1
	s_waitcnt lgkmcnt(0)
	v_mfma_scale_f32_16x16x128_f8f6f4 v[76:79], v[158:165], v[202:209], v[76:79], v211, v212 op_sel_hi:[0,0,0]
	v_mfma_scale_f32_16x16x128_f8f6f4 v[72:75], v[166:173], v[202:209], v[72:75], v211, v212 op_sel_hi:[0,0,0]
	v_mfma_scale_f32_16x16x128_f8f6f4 v[44:47], v[158:165], v[220:227], v[44:47], v211, v212 op_sel_hi:[0,0,0]
	v_mfma_scale_f32_16x16x128_f8f6f4 v[40:43], v[166:173], v[220:227], v[40:43], v211, v212 op_sel_hi:[0,0,0]
	v_mfma_scale_f32_16x16x128_f8f6f4 v[20:23], v[158:165], v[236:243], v[20:23], v211, v212 op_sel_hi:[0,0,0]
	v_mfma_scale_f32_16x16x128_f8f6f4 v[16:19], v[166:173], v[236:243], v[16:19], v211, v212 op_sel_hi:[0,0,0]
	v_mfma_scale_f32_16x16x128_f8f6f4 v[8:11], v[158:165], v[244:251], v[8:11], v211, v212 op_sel_hi:[0,0,0]
	v_mfma_scale_f32_16x16x128_f8f6f4 v[4:7], v[166:173], v[244:251], v[4:7], v211, v212 op_sel_hi:[0,0,0]
	s_setprio 0
	s_setprio 1
	v_mfma_scale_f32_16x16x128_f8f6f4 v[92:95], v[182:189], v[202:209], v[92:95], v211, v212 op_sel_hi:[0,0,0]
	v_mfma_scale_f32_16x16x128_f8f6f4 v[88:91], v[190:197], v[202:209], v[88:91], v211, v212 op_sel_hi:[0,0,0]
	v_mfma_scale_f32_16x16x128_f8f6f4 v[60:63], v[182:189], v[220:227], v[60:63], v211, v212 op_sel_hi:[0,0,0]
	v_mfma_scale_f32_16x16x128_f8f6f4 v[56:59], v[190:197], v[220:227], v[56:59], v211, v212 op_sel_hi:[0,0,0]
	v_mfma_scale_f32_16x16x128_f8f6f4 v[28:31], v[182:189], v[236:243], v[28:31], v211, v212 op_sel_hi:[0,0,0]
	v_mfma_scale_f32_16x16x128_f8f6f4 v[24:27], v[190:197], v[236:243], v[24:27], v211, v212 op_sel_hi:[0,0,0]
	v_mfma_scale_f32_16x16x128_f8f6f4 v[12:15], v[182:189], v[244:251], v[12:15], v211, v212 op_sel_hi:[0,0,0]
	v_mfma_scale_f32_16x16x128_f8f6f4 v[0:3], v[190:197], v[244:251], v[0:3], v211, v212 op_sel_hi:[0,0,0]
	s_setprio 0
	s_barrier
; __device__ __forceinline__ unsigned pk4f8(float a, float b, float c, float d) { int w = 0; w = __builtin_amdgcn_cvt_pk_fp8_f32(a, b, w, false); w = __builtin_amdgcn_cvt_pk_fp8_f32(c, d, w, true); return (unsigned)w; }
;     __device__ __forceinline__ void operator()(const f32x4 (&acc)[2][2][4][2], const Unit& u, int wr, int wc, int fr, int fq) const {
;         unsigned char* base = O; int pm = u.pm; int ld = ldc; if (pm >= pm_split) { base = O2; pm -= pm_off2; ld = ldc2; }
;         const int row0 = pm * BM + wr * 64 + fr; const int col0 = u.pn * BM + wc * 32 + ((fq & 1) ? HALF + 8 * (fq - 1) : 8 * fq);
; #pragma unroll
;         for (int ai = 0; ai < 2; ++ai)
; #pragma unroll
;             for (int m = 0; m < 4; ++m) { unsigned char* rowp = base + (size_t)(row0 + ai * HALF + m * 16) * ld + col0;
;                 const f32x4 p0 = acc[ai][0][m][0] * scale, p1 = acc[ai][0][m][1] * scale, q0 = acc[ai][1][m][0] * scale, q1 = acc[ai][1][m][1] * scale;
;                 unsigned ax = pk4f8(p0[0], p0[1], p0[2], p0[3]), ay = pk4f8(p1[0], p1[1], p1[2], p1[3]), bx = pk4f8(q0[0], q0[1], q0[2], q0[3]), by = pk4f8(q1[0], q1[1], q1[2], q1[3]);
;                 { auto r = __builtin_amdgcn_permlane16_swap(ax, bx, false, false); ax = r[0]; bx = r[1]; }
;                 { auto r = __builtin_amdgcn_permlane16_swap(ay, by, false, false); ay = r[0]; by = r[1]; }
;                 u32x4 w; w.x = ax; w.y = ay; w.z = bx; w.w = by;
;                 *(u32x4*)rowp = w; }
	s_cmpk_lt_i32 s41, 0x480
	v_mov_b32_e32 v139, v200
	s_cselect_b32 s0, 0, 0xfffffb80
	s_mov_b32 s1, 0x18c00000
	s_cselect_b32 s1, s1, 0x2ae00000
	s_add_i32 s2, s0, s41
	v_ashrrev_i32_e32 v158, 1, v139
	s_add_u32 s0, s6, s1
	v_and_b32_e32 v138, 16, v139
	v_and_b32_e32 v158, -8, v158
	s_addc_u32 s1, s7, 0
	s_lshl_b32 s3, s42, 8
	v_add_u32_e32 v159, 0x78, v158
	v_cmp_eq_u32_e32 vcc, 0, v138
	v_and_or_b32 v139, v139, 15, v140
	s_or_b32 s3, s3, s16
	v_cndmask_b32_e32 v138, v159, v158, vcc
	v_lshl_add_u32 v158, s2, 8, v139
	s_mov_b32 s2, 0x41800000
	v_pk_mul_f32 v[162:163], v[114:115], s[2:3] op_sel_hi:[1,0]
	v_pk_mul_f32 v[114:115], v[112:113], s[2:3] op_sel_hi:[1,0]
	v_pk_mul_f32 v[116:117], v[116:117], s[2:3] op_sel_hi:[1,0]
	v_pk_mul_f32 v[124:125], v[124:125], s[2:3] op_sel_hi:[1,0]
	v_pk_mul_f32 v[120:121], v[120:121], s[2:3] op_sel_hi:[1,0]
	v_cvt_pk_fp8_f32 v113, v114, v115
	v_cvt_pk_fp8_f32 v112, v116, v117
	v_cvt_pk_fp8_f32 v114, v124, v125
	v_cvt_pk_fp8_f32 v115, v120, v121
	v_pk_mul_f32 v[118:119], v[118:119], s[2:3] op_sel_hi:[1,0]
	v_pk_mul_f32 v[126:127], v[126:127], s[2:3] op_sel_hi:[1,0]
	v_pk_mul_f32 v[122:123], v[122:123], s[2:3] op_sel_hi:[1,0]
	v_cvt_pk_fp8_f32 v112, v118, v119 op_sel:[0,0,1]
	v_cvt_pk_fp8_f32 v114, v126, v127 op_sel:[0,0,1]
	v_cvt_pk_fp8_f32 v113, v162, v163 op_sel:[0,0,1]
	v_cvt_pk_fp8_f32 v115, v122, v123 op_sel:[0,0,1]
	v_add_u32_e32 v138, s3, v138
	v_ashrrev_i32_e32 v139, 31, v138
	v_ashrrev_i32_e32 v159, 31, v158
	v_lshl_add_u64 v[160:161], s[0:1], 0, v[138:139]
	v_lshlrev_b64 v[138:139], 10, v[158:159]
	v_lshl_add_u64 v[138:139], v[160:161], 0, v[138:139]
	v_permlane16_swap_b32_e32 v112, v114
	v_permlane16_swap_b32_e32 v113, v115
	global_store_dwordx4 v[138:139], v[112:115], off
	v_pk_mul_f32 v[100:101], v[100:101], s[2:3] op_sel_hi:[1,0]
	v_pk_mul_f32 v[108:109], v[108:109], s[2:3] op_sel_hi:[1,0]
	v_pk_mul_f32 v[114:115], v[98:99], s[2:3] op_sel_hi:[1,0]
	v_pk_mul_f32 v[98:99], v[96:97], s[2:3] op_sel_hi:[1,0]
	v_pk_mul_f32 v[104:105], v[104:105], s[2:3] op_sel_hi:[1,0]
	v_cvt_pk_fp8_f32 v97, v98, v99
	v_cvt_pk_fp8_f32 v96, v100, v101
	v_cvt_pk_fp8_f32 v98, v108, v109
	v_cvt_pk_fp8_f32 v99, v104, v105
	v_pk_mul_f32 v[102:103], v[102:103], s[2:3] op_sel_hi:[1,0]
	v_pk_mul_f32 v[110:111], v[110:111], s[2:3] op_sel_hi:[1,0]
	v_pk_mul_f32 v[106:107], v[106:107], s[2:3] op_sel_hi:[1,0]
	v_cvt_pk_fp8_f32 v96, v102, v103 op_sel:[0,0,1]
	v_cvt_pk_fp8_f32 v98, v110, v111 op_sel:[0,0,1]
	v_cvt_pk_fp8_f32 v97, v114, v115 op_sel:[0,0,1]
	v_cvt_pk_fp8_f32 v99, v106, v107 op_sel:[0,0,1]
	v_or_b32_e32 v112, 16, v158
	v_ashrrev_i32_e32 v113, 31, v112
	v_lshlrev_b64 v[112:113], 10, v[112:113]
	v_lshl_add_u64 v[112:113], v[160:161], 0, v[112:113]
	v_permlane16_swap_b32_e32 v96, v98
	v_permlane16_swap_b32_e32 v97, v99
	global_store_dwordx4 v[112:113], v[96:99], off
	v_pk_mul_f32 v[68:69], v[68:69], s[2:3] op_sel_hi:[1,0]
	v_pk_mul_f32 v[84:85], v[84:85], s[2:3] op_sel_hi:[1,0]
	v_pk_mul_f32 v[98:99], v[66:67], s[2:3] op_sel_hi:[1,0]
	v_pk_mul_f32 v[66:67], v[64:65], s[2:3] op_sel_hi:[1,0]
	v_pk_mul_f32 v[80:81], v[80:81], s[2:3] op_sel_hi:[1,0]
	v_cvt_pk_fp8_f32 v65, v66, v67
	v_cvt_pk_fp8_f32 v64, v68, v69
	v_cvt_pk_fp8_f32 v66, v84, v85
	v_cvt_pk_fp8_f32 v67, v80, v81
	v_pk_mul_f32 v[70:71], v[70:71], s[2:3] op_sel_hi:[1,0]
	v_pk_mul_f32 v[86:87], v[86:87], s[2:3] op_sel_hi:[1,0]
	v_pk_mul_f32 v[82:83], v[82:83], s[2:3] op_sel_hi:[1,0]
	v_cvt_pk_fp8_f32 v64, v70, v71 op_sel:[0,0,1]
	v_cvt_pk_fp8_f32 v66, v86, v87 op_sel:[0,0,1]
	v_cvt_pk_fp8_f32 v65, v98, v99 op_sel:[0,0,1]
	v_cvt_pk_fp8_f32 v67, v82, v83 op_sel:[0,0,1]
	v_or_b32_e32 v96, 32, v158
	v_ashrrev_i32_e32 v97, 31, v96
	v_lshlrev_b64 v[96:97], 10, v[96:97]
	v_lshl_add_u64 v[96:97], v[160:161], 0, v[96:97]
	v_permlane16_swap_b32_e32 v64, v66
	v_permlane16_swap_b32_e32 v65, v67
	global_store_dwordx4 v[96:97], v[64:67], off
	v_pk_mul_f32 v[36:37], v[36:37], s[2:3] op_sel_hi:[1,0]
	v_pk_mul_f32 v[52:53], v[52:53], s[2:3] op_sel_hi:[1,0]
	v_pk_mul_f32 v[66:67], v[34:35], s[2:3] op_sel_hi:[1,0]
	v_pk_mul_f32 v[34:35], v[32:33], s[2:3] op_sel_hi:[1,0]
	v_pk_mul_f32 v[48:49], v[48:49], s[2:3] op_sel_hi:[1,0]
	v_cvt_pk_fp8_f32 v33, v34, v35
	v_cvt_pk_fp8_f32 v32, v36, v37
	v_cvt_pk_fp8_f32 v34, v52, v53
	v_cvt_pk_fp8_f32 v35, v48, v49
	v_pk_mul_f32 v[38:39], v[38:39], s[2:3] op_sel_hi:[1,0]
	v_pk_mul_f32 v[54:55], v[54:55], s[2:3] op_sel_hi:[1,0]
	v_pk_mul_f32 v[50:51], v[50:51], s[2:3] op_sel_hi:[1,0]
	v_cvt_pk_fp8_f32 v32, v38, v39 op_sel:[0,0,1]
; __device__ __forceinline__ unsigned pk4f8(float a, float b, float c, float d) { int w = 0; w = __builtin_amdgcn_cvt_pk_fp8_f32(a, b, w, false); w = __builtin_amdgcn_cvt_pk_fp8_f32(c, d, w, true); return (unsigned)w; }
;     __device__ __forceinline__ void operator()(const f32x4 (&acc)[2][2][4][2], const Unit& u, int wr, int wc, int fr, int fq) const {
;         unsigned char* base = O; int pm = u.pm; int ld = ldc; if (pm >= pm_split) { base = O2; pm -= pm_off2; ld = ldc2; }
;         const int row0 = pm * BM + wr * 64 + fr; const int col0 = u.pn * BM + wc * 32 + ((fq & 1) ? HALF + 8 * (fq - 1) : 8 * fq);
; #pragma unroll
;         for (int ai = 0; ai < 2; ++ai)
; #pragma unroll
;             for (int m = 0; m < 4; ++m) { unsigned char* rowp = base + (size_t)(row0 + ai * HALF + m * 16) * ld + col0;
;                 const f32x4 p0 = acc[ai][0][m][0] * scale, p1 = acc[ai][0][m][1] * scale, q0 = acc[ai][1][m][0] * scale, q1 = acc[ai][1][m][1] * scale;
;                 unsigned ax = pk4f8(p0[0], p0[1], p0[2], p0[3]), ay = pk4f8(p1[0], p1[1], p1[2], p1[3]), bx = pk4f8(q0[0], q0[1], q0[2], q0[3]), by = pk4f8(q1[0], q1[1], q1[2], q1[3]);
;                 { auto r = __builtin_amdgcn_permlane16_swap(ax, bx, false, false); ax = r[0]; bx = r[1]; }
;                 { auto r = __builtin_amdgcn_permlane16_swap(ay, by, false, false); ay = r[0]; by = r[1]; }
;                 u32x4 w; w.x = ax; w.y = ay; w.z = bx; w.w = by;
;                 *(u32x4*)rowp = w; }
	v_cvt_pk_fp8_f32 v34, v54, v55 op_sel:[0,0,1]
	v_cvt_pk_fp8_f32 v33, v66, v67 op_sel:[0,0,1]
	v_cvt_pk_fp8_f32 v35, v50, v51 op_sel:[0,0,1]
	v_or_b32_e32 v64, 48, v158
	v_ashrrev_i32_e32 v65, 31, v64
	v_lshlrev_b64 v[64:65], 10, v[64:65]
	v_lshl_add_u64 v[64:65], v[160:161], 0, v[64:65]
	v_permlane16_swap_b32_e32 v32, v34
	v_permlane16_swap_b32_e32 v33, v35
	global_store_dwordx4 v[64:65], v[32:35], off
	v_pk_mul_f32 v[48:49], v[72:73], s[2:3] op_sel_hi:[1,0]
	v_pk_mul_f32 v[52:53], v[92:93], s[2:3] op_sel_hi:[1,0]
	v_pk_mul_f32 v[34:35], v[76:77], s[2:3] op_sel_hi:[1,0]
	v_pk_mul_f32 v[64:65], v[88:89], s[2:3] op_sel_hi:[1,0]
	v_cvt_pk_fp8_f32 v32, v34, v35
	v_cvt_pk_fp8_f32 v33, v48, v49
	v_cvt_pk_fp8_f32 v34, v52, v53
	v_cvt_pk_fp8_f32 v35, v64, v65
	v_pk_mul_f32 v[36:37], v[78:79], s[2:3] op_sel_hi:[1,0]
	v_pk_mul_f32 v[38:39], v[74:75], s[2:3] op_sel_hi:[1,0]
	v_pk_mul_f32 v[50:51], v[94:95], s[2:3] op_sel_hi:[1,0]
	v_pk_mul_f32 v[54:55], v[90:91], s[2:3] op_sel_hi:[1,0]
	v_cvt_pk_fp8_f32 v32, v36, v37 op_sel:[0,0,1]
	v_cvt_pk_fp8_f32 v34, v50, v51 op_sel:[0,0,1]
	v_cvt_pk_fp8_f32 v33, v38, v39 op_sel:[0,0,1]
	v_cvt_pk_fp8_f32 v35, v54, v55 op_sel:[0,0,1]
	s_mov_b32 s0, 0x20000
	v_add_co_u32_e32 v36, vcc, s0, v138
	v_permlane16_swap_b32_e32 v32, v34
	v_permlane16_swap_b32_e32 v33, v35
	v_addc_co_u32_e32 v37, vcc, 0, v139, vcc
	global_store_dwordx4 v[36:37], v[32:35], off
	v_pk_mul_f32 v[40:41], v[40:41], s[2:3] op_sel_hi:[1,0]
	v_pk_mul_f32 v[48:49], v[56:57], s[2:3] op_sel_hi:[1,0]
	v_pk_mul_f32 v[34:35], v[44:45], s[2:3] op_sel_hi:[1,0]
	v_pk_mul_f32 v[44:45], v[60:61], s[2:3] op_sel_hi:[1,0]
	v_cvt_pk_fp8_f32 v32, v34, v35
	v_cvt_pk_fp8_f32 v33, v40, v41
	v_cvt_pk_fp8_f32 v34, v44, v45
	v_cvt_pk_fp8_f32 v35, v48, v49
	v_pk_mul_f32 v[36:37], v[46:47], s[2:3] op_sel_hi:[1,0]
	v_pk_mul_f32 v[38:39], v[42:43], s[2:3] op_sel_hi:[1,0]
	v_pk_mul_f32 v[42:43], v[62:63], s[2:3] op_sel_hi:[1,0]
	v_pk_mul_f32 v[46:47], v[58:59], s[2:3] op_sel_hi:[1,0]
	v_cvt_pk_fp8_f32 v32, v36, v37 op_sel:[0,0,1]
	v_cvt_pk_fp8_f32 v34, v42, v43 op_sel:[0,0,1]
	v_cvt_pk_fp8_f32 v33, v38, v39 op_sel:[0,0,1]
	v_cvt_pk_fp8_f32 v35, v46, v47 op_sel:[0,0,1]
	s_mov_b32 s0, 0x24000
	v_add_co_u32_e32 v36, vcc, s0, v138
	v_permlane16_swap_b32_e32 v32, v34
	v_permlane16_swap_b32_e32 v33, v35
	v_addc_co_u32_e32 v37, vcc, 0, v139, vcc
	global_store_dwordx4 v[36:37], v[32:35], off
	v_pk_mul_f32 v[20:21], v[20:21], s[2:3] op_sel_hi:[1,0]
	v_pk_mul_f32 v[28:29], v[28:29], s[2:3] op_sel_hi:[1,0]
	v_pk_mul_f32 v[32:33], v[18:19], s[2:3] op_sel_hi:[1,0]
	v_pk_mul_f32 v[18:19], v[16:17], s[2:3] op_sel_hi:[1,0]
	v_pk_mul_f32 v[24:25], v[24:25], s[2:3] op_sel_hi:[1,0]
	v_cvt_pk_fp8_f32 v17, v18, v19
	v_cvt_pk_fp8_f32 v16, v20, v21
	v_cvt_pk_fp8_f32 v18, v28, v29
	v_cvt_pk_fp8_f32 v19, v24, v25
	v_pk_mul_f32 v[22:23], v[22:23], s[2:3] op_sel_hi:[1,0]
	v_pk_mul_f32 v[30:31], v[30:31], s[2:3] op_sel_hi:[1,0]
	v_pk_mul_f32 v[26:27], v[26:27], s[2:3] op_sel_hi:[1,0]
	v_cvt_pk_fp8_f32 v16, v22, v23 op_sel:[0,0,1]
	v_cvt_pk_fp8_f32 v18, v30, v31 op_sel:[0,0,1]
	v_cvt_pk_fp8_f32 v17, v32, v33 op_sel:[0,0,1]
	v_cvt_pk_fp8_f32 v19, v26, v27 op_sel:[0,0,1]
	s_mov_b32 s0, 0x28000
	v_add_co_u32_e32 v20, vcc, s0, v138
	v_permlane16_swap_b32_e32 v16, v18
	v_permlane16_swap_b32_e32 v17, v19
	v_addc_co_u32_e32 v21, vcc, 0, v139, vcc
	global_store_dwordx4 v[20:21], v[16:19], off
	v_pk_mul_f32 v[8:9], v[8:9], s[2:3] op_sel_hi:[1,0]
	v_pk_mul_f32 v[4:5], v[4:5], s[2:3] op_sel_hi:[1,0]
	v_pk_mul_f32 v[12:13], v[12:13], s[2:3] op_sel_hi:[1,0]
	v_pk_mul_f32 v[16:17], v[2:3], s[2:3] op_sel_hi:[1,0]
	v_pk_mul_f32 v[18:19], v[0:1], s[2:3] op_sel_hi:[1,0]
	v_cvt_pk_fp8_f32 v0, v8, v9
	v_cvt_pk_fp8_f32 v1, v4, v5
	v_cvt_pk_fp8_f32 v2, v12, v13
	v_cvt_pk_fp8_f32 v3, v18, v19
	v_pk_mul_f32 v[10:11], v[10:11], s[2:3] op_sel_hi:[1,0]
	v_pk_mul_f32 v[6:7], v[6:7], s[2:3] op_sel_hi:[1,0]
	v_pk_mul_f32 v[14:15], v[14:15], s[2:3] op_sel_hi:[1,0]
	v_cvt_pk_fp8_f32 v0, v10, v11 op_sel:[0,0,1]
	v_cvt_pk_fp8_f32 v2, v14, v15 op_sel:[0,0,1]
	v_cvt_pk_fp8_f32 v1, v6, v7 op_sel:[0,0,1]
	v_cvt_pk_fp8_f32 v3, v16, v17 op_sel:[0,0,1]
	v_add_co_u32_e32 v4, vcc, 0x2c000, v138
	v_permlane16_swap_b32_e32 v0, v2
	s_nop 0
	v_addc_co_u32_e32 v5, vcc, 0, v139, vcc
	v_permlane16_swap_b32_e32 v1, v3
	s_add_i32 s40, s40, 1
	s_andn2_b64 vcc, exec, s[26:27]
	s_mov_b32 s42, s22
	s_mov_b32 s41, s14
	s_mov_b64 s[0:1], s[36:37]
	global_store_dwordx4 v[4:5], v[0:3], off
	s_cbranch_vccz .LBB0_1638
